# v22 + GLA merge: the loop-top drain of the previous row group's stores removed (next group's loads issue while the stores retire)
# baseline (speedup 1.0000x reference)
.LBB0_565:
	v_lshl_add_u64 v[4:5], s[8:9], 0, v[104:105]
	v_add_co_u32_e32 v116, vcc, 0x13000000, v4
	s_nop 0
	v_lshl_add_u64 v[12:13], s[8:9], 0, v[108:109]
	v_addc_co_u32_e32 v117, vcc, 0, v5, vcc
	v_add_co_u32_e32 v6, vcc, 0x17400000, v4
	global_load_dwordx4 v[0:3], v[102:103], off offset:16
	global_load_dwordx4 v[8:11], v[102:103], off
	v_addc_co_u32_e32 v7, vcc, 0, v5, vcc
	global_load_dwordx4 v[94:97], v[116:117], off nt
	global_load_dwordx4 v[98:101], v[6:7], off nt
	v_add_co_u32_e32 v14, vcc, 0x6401000, v12
	s_mov_b32 s0, 0x13000000
	s_nop 0
	v_addc_co_u32_e32 v15, vcc, 0, v13, vcc
	global_load_dwordx4 v[124:127], v[14:15], off nt
	v_lshl_add_u64 v[14:15], s[8:9], 0, v[110:111]
	v_add_co_u32_e32 v16, vcc, s0, v14
	s_mov_b32 s0, 0x17400000
	s_nop 0
	v_addc_co_u32_e32 v17, vcc, 0, v15, vcc
	v_add_co_u32_e32 v18, vcc, s42, v14
	v_lshl_add_u64 v[118:119], s[8:9], 0, v[106:107]
	s_nop 0
	v_addc_co_u32_e32 v19, vcc, 0, v15, vcc
	v_add_co_u32_e32 v20, vcc, s0, v14
	s_mov_b32 s0, 0x6401000
	s_nop 0
	v_addc_co_u32_e32 v21, vcc, 0, v15, vcc
	v_add_co_u32_e32 v14, vcc, s43, v14
	global_load_dwordx4 v[86:89], v[18:19], off offset:-4096 nt
	s_nop 0
	v_addc_co_u32_e32 v15, vcc, 0, v15, vcc
	v_add_co_u32_e32 v22, vcc, s0, v118
	global_load_dwordx4 v[90:93], v[14:15], off offset:-4096 nt
	s_nop 0
	v_addc_co_u32_e32 v23, vcc, 0, v119, vcc
	global_load_dwordx4 v[82:85], v[22:23], off nt
	global_load_dwordx4 v[78:81], v[116:117], off offset:2048 nt
	global_load_dwordx4 v[74:77], v[6:7], off offset:2048 nt
	v_add_co_u32_e32 v6, vcc, s49, v12
	s_add_i32 s6, s6, s50
	s_nop 0
	v_addc_co_u32_e32 v7, vcc, 0, v13, vcc
	global_load_dwordx4 v[70:73], v[6:7], off offset:2048 nt
	global_load_dwordx4 v[66:69], v[16:17], off offset:2048 nt
	global_load_dwordx4 v[60:63], v[20:21], off offset:2048 nt
	v_add_co_u32_e32 v6, vcc, s49, v118
	v_lshl_add_u64 v[104:105], v[104:105], 0, s[34:35]
	s_nop 0
	v_addc_co_u32_e32 v7, vcc, 0, v119, vcc
	v_add_co_u32_e32 v112, vcc, s42, v4
	global_load_dwordx4 v[56:59], v[6:7], off offset:2048 nt
	s_nop 0
	v_addc_co_u32_e32 v113, vcc, 0, v5, vcc
	v_add_co_u32_e32 v4, vcc, s43, v4
	global_load_dwordx4 v[48:51], v[112:113], off nt
	s_nop 0
	v_addc_co_u32_e32 v5, vcc, 0, v5, vcc
	global_load_dwordx4 v[52:55], v[4:5], off nt
	v_add_co_u32_e32 v6, vcc, s10, v12
	v_lshl_add_u64 v[106:107], v[106:107], 0, s[44:45]
	s_nop 0
	v_addc_co_u32_e32 v7, vcc, 0, v13, vcc
	s_waitcnt lgkmcnt(0)
	global_load_dwordx4 v[44:47], v[6:7], off nt
	global_load_dwordx4 v[40:43], v[18:19], off nt
	global_load_dwordx4 v[36:39], v[14:15], off nt
	v_add_co_u32_e32 v6, vcc, s10, v118
	v_lshl_add_u64 v[108:109], v[108:109], 0, s[44:45]
	s_nop 0
	v_addc_co_u32_e32 v7, vcc, 0, v119, vcc
	global_load_dwordx4 v[32:35], v[6:7], off nt
	global_load_dwordx4 v[28:31], v[112:113], off offset:2048 nt
	global_load_dwordx4 v[24:27], v[4:5], off offset:2048 nt
	v_add_co_u32_e32 v4, vcc, s11, v12
	v_lshl_add_u64 v[110:111], v[110:111], 0, s[34:35]
	s_nop 0
	v_addc_co_u32_e32 v5, vcc, 0, v13, vcc
	global_load_dwordx4 v[20:23], v[4:5], off offset:2048 nt
	s_nop 0
	global_load_dwordx4 v[16:19], v[18:19], off offset:2048 nt
	s_nop 0
	global_load_dwordx4 v[12:15], v[14:15], off offset:2048 nt
	v_add_co_u32_e32 v4, vcc, s11, v118
	s_cmp_lt_i32 s6, 0x8800
	s_nop 0
	v_addc_co_u32_e32 v5, vcc, 0, v119, vcc
	s_waitcnt vmcnt(0)
	v_lshlrev_b32_e32 v119, 16, v95
	v_lshlrev_b32_e32 v118, 16, v94
	v_lshlrev_b32_e32 v121, 16, v99
	v_lshlrev_b32_e32 v120, 16, v98
	v_pk_add_f32 v[118:119], v[118:119], v[120:121]
	v_and_b32_e32 v95, 0xffff0000, v95
	v_and_b32_e32 v94, 0xffff0000, v94
	v_and_b32_e32 v99, 0xffff0000, v99
	v_and_b32_e32 v98, 0xffff0000, v98
	v_pk_add_f32 v[98:99], v[94:95], v[98:99]
	v_pk_mul_f32 v[94:95], v[118:119], v[118:119]
	v_lshlrev_b32_e32 v114, 16, v124
	v_pk_fma_f32 v[132:133], v[98:99], v[98:99], v[94:95]
	v_mul_f32_e32 v94, 0xbfb8aa3b, v114
	v_and_b32_e32 v124, 0xffff0000, v124
	v_lshlrev_b32_e32 v65, 16, v125
	v_exp_f32_e32 v120, v94
	v_mul_f32_e32 v94, 0xbfb8aa3b, v124
	v_exp_f32_e32 v122, v94
	v_mov_b32_e32 v94, v8
	v_mul_f32_e32 v8, 0xbfb8aa3b, v65
	v_exp_f32_e32 v121, v8
	v_mov_b32_e32 v95, v10
	v_and_b32_e32 v125, 0xffff0000, v125
	v_and_b32_e32 v130, 0xffff0000, v126
	v_pk_add_f32 v[120:121], v[120:121], 1.0 op_sel_hi:[1,0]
	global_load_dwordx4 v[4:7], v[4:5], off offset:2048 nt
	v_div_scale_f32 v8, s[0:1], v121, v121, v65
	v_rcp_f32_e32 v10, v8
	v_and_b32_e32 v137, 0xffff0000, v82
	v_fma_f32 v123, -v8, v10, 1.0
	v_fmac_f32_e32 v10, v123, v10
	v_div_scale_f32 v123, vcc, v65, v121, v65
	v_mul_f32_e32 v128, v123, v10
	v_fma_f32 v129, -v8, v128, v123
	v_fmac_f32_e32 v128, v129, v10
	v_fma_f32 v8, -v8, v128, v123
	v_div_fmas_f32 v8, v8, v10, v128
	v_div_fixup_f32 v121, v8, v121, v65
	v_div_scale_f32 v8, s[0:1], v120, v120, v114
	v_rcp_f32_e32 v10, v8
	v_and_b32_e32 v136, 0xffff0000, v83
	v_fma_f32 v65, -v8, v10, 1.0
	v_fmac_f32_e32 v10, v65, v10
	v_div_scale_f32 v65, vcc, v114, v120, v114
	v_mul_f32_e32 v123, v65, v10
	v_fma_f32 v128, -v8, v123, v65
	v_fmac_f32_e32 v123, v128, v10
	v_fma_f32 v8, -v8, v123, v65
	v_div_fmas_f32 v8, v8, v10, v123
	v_div_fixup_f32 v120, v8, v120, v114
	v_mul_f32_e32 v8, 0xbfb8aa3b, v125
	v_exp_f32_e32 v123, v8
	v_mov_b32_e32 v10, v9
	v_pk_add_f32 v[8:9], v[122:123], 1.0 op_sel_hi:[1,0]
	s_nop 0
	v_div_scale_f32 v65, s[0:1], v9, v9, v125
	v_rcp_f32_e32 v114, v65
	s_nop 0
	v_fma_f32 v122, -v65, v114, 1.0
	v_fmac_f32_e32 v114, v122, v114
	v_div_scale_f32 v122, vcc, v125, v9, v125
	v_mul_f32_e32 v123, v122, v114
	v_fma_f32 v128, -v65, v123, v122
	v_fmac_f32_e32 v123, v128, v114
	v_fma_f32 v65, -v65, v123, v122
	v_div_fmas_f32 v65, v65, v114, v123
	v_div_fixup_f32 v123, v65, v9, v125
	v_div_scale_f32 v9, s[0:1], v8, v8, v124
	v_rcp_f32_e32 v65, v9
	v_and_b32_e32 v128, 0xffff0000, v127
	v_fma_f32 v114, -v9, v65, 1.0
	v_fmac_f32_e32 v65, v114, v65
	v_div_scale_f32 v114, vcc, v124, v8, v124
	v_mul_f32_e32 v122, v114, v65
	v_fma_f32 v125, -v9, v122, v114
	v_fmac_f32_e32 v122, v125, v65
	v_fma_f32 v9, -v9, v122, v114
	v_div_fmas_f32 v9, v9, v65, v122
	v_div_fixup_f32 v122, v9, v8, v124
	v_lshlrev_b32_e32 v9, 16, v97
	v_lshlrev_b32_e32 v8, 16, v96
	v_lshlrev_b32_e32 v125, 16, v101
	v_lshlrev_b32_e32 v124, 16, v100
	v_pk_add_f32 v[124:125], v[8:9], v[124:125]
	v_and_b32_e32 v9, 0xffff0000, v97
	v_and_b32_e32 v8, 0xffff0000, v96
	v_and_b32_e32 v97, 0xffff0000, v101
	v_and_b32_e32 v96, 0xffff0000, v100
	v_pk_add_f32 v[96:97], v[8:9], v[96:97]
	v_pk_mul_f32 v[8:9], v[124:125], v[124:125]
	v_lshlrev_b32_e32 v114, 16, v126
	v_pk_fma_f32 v[134:135], v[96:97], v[96:97], v[8:9]
	v_mul_f32_e32 v8, 0xbfb8aa3b, v114
	v_lshlrev_b32_e32 v65, 16, v127
	v_exp_f32_e32 v100, v8
	v_mul_f32_e32 v8, 0xbfb8aa3b, v130
	v_exp_f32_e32 v126, v8
	v_mov_b32_e32 v8, v0
	v_mul_f32_e32 v0, 0xbfb8aa3b, v65
	v_exp_f32_e32 v101, v0
	v_mov_b32_e32 v9, v2
	v_pk_add_f32 v[100:101], v[100:101], 1.0 op_sel_hi:[1,0]
	s_nop 0
	v_div_scale_f32 v0, s[0:1], v101, v101, v65
	v_rcp_f32_e32 v2, v0
	s_nop 0
	v_fma_f32 v127, -v0, v2, 1.0
	v_fmac_f32_e32 v2, v127, v2
	v_div_scale_f32 v127, vcc, v65, v101, v65
	v_mul_f32_e32 v129, v127, v2
	v_fma_f32 v131, -v0, v129, v127
	v_fmac_f32_e32 v129, v131, v2
	v_fma_f32 v0, -v0, v129, v127
	v_div_fmas_f32 v0, v0, v2, v129
	v_div_fixup_f32 v101, v0, v101, v65
	v_div_scale_f32 v0, s[0:1], v100, v100, v114
	v_rcp_f32_e32 v2, v0
	s_nop 0
	v_fma_f32 v65, -v0, v2, 1.0
	v_fmac_f32_e32 v2, v65, v2
	v_div_scale_f32 v65, vcc, v114, v100, v114
	v_mul_f32_e32 v127, v65, v2
	v_fma_f32 v129, -v0, v127, v65
	v_fmac_f32_e32 v127, v129, v2
	v_fma_f32 v0, -v0, v127, v65
	v_div_fmas_f32 v0, v0, v2, v127
	v_div_fixup_f32 v100, v0, v100, v114
	v_mul_f32_e32 v0, 0xbfb8aa3b, v128
	v_exp_f32_e32 v127, v0
	v_mov_b32_e32 v2, v1
	v_pk_add_f32 v[0:1], v[126:127], 1.0 op_sel_hi:[1,0]
	s_nop 0
	v_div_scale_f32 v65, s[0:1], v1, v1, v128
	v_rcp_f32_e32 v114, v65
	s_nop 0
	v_fma_f32 v126, -v65, v114, 1.0
	v_fmac_f32_e32 v114, v126, v114
	v_div_scale_f32 v126, vcc, v128, v1, v128
	v_mul_f32_e32 v127, v126, v114
	v_fma_f32 v129, -v65, v127, v126
	v_fmac_f32_e32 v127, v129, v114
	v_fma_f32 v65, -v65, v127, v126
	v_div_fmas_f32 v65, v65, v114, v127
	v_div_fixup_f32 v129, v65, v1, v128
	v_div_scale_f32 v1, s[0:1], v0, v0, v130
	v_rcp_f32_e32 v65, v1
	s_nop 0
	v_fma_f32 v114, -v1, v65, 1.0
	v_fmac_f32_e32 v65, v114, v65
	v_div_scale_f32 v114, vcc, v130, v0, v130
	v_mul_f32_e32 v126, v114, v65
	v_fma_f32 v127, -v1, v126, v114
	v_fmac_f32_e32 v126, v127, v65
	v_fma_f32 v1, -v1, v126, v114
	v_div_fmas_f32 v1, v1, v65, v126
	v_div_fixup_f32 v128, v1, v0, v130
	v_lshlrev_b32_e32 v1, 16, v87
	v_lshlrev_b32_e32 v0, 16, v86
	v_lshlrev_b32_e32 v127, 16, v91
	v_lshlrev_b32_e32 v126, 16, v90
	v_lshlrev_b32_e32 v65, 16, v83
	v_lshlrev_b32_e32 v114, 16, v82
	v_mul_f32_e32 v82, 0xbfb8aa3b, v137
	v_pk_add_f32 v[126:127], v[0:1], v[126:127]
	v_and_b32_e32 v0, 0xffff0000, v86
	v_and_b32_e32 v86, 0xffff0000, v90
	v_mul_f32_e32 v90, 0xbfb8aa3b, v114
	v_exp_f32_e32 v130, v82
	v_mul_f32_e32 v82, 0xbfb8aa3b, v65
	v_and_b32_e32 v1, 0xffff0000, v87
	v_and_b32_e32 v87, 0xffff0000, v91
	v_exp_f32_e32 v90, v90
	v_exp_f32_e32 v91, v82
	v_pk_add_f32 v[86:87], v[0:1], v[86:87]
	v_pk_mul_f32 v[0:1], v[126:127], v[126:127]
	v_pk_add_f32 v[82:83], v[90:91], 1.0 op_sel_hi:[1,0]
	s_nop 0
	v_div_scale_f32 v90, s[0:1], v83, v83, v65
	v_rcp_f32_e32 v91, v90
	v_pk_fma_f32 v[0:1], v[86:87], v[86:87], v[0:1]
	v_fma_f32 v131, -v90, v91, 1.0
	v_fmac_f32_e32 v91, v131, v91
	v_div_scale_f32 v131, vcc, v65, v83, v65
	v_mul_f32_e32 v138, v131, v91
	v_fma_f32 v139, -v90, v138, v131
	v_fmac_f32_e32 v138, v139, v91
	v_fma_f32 v90, -v90, v138, v131
	v_div_fmas_f32 v90, v90, v91, v138
	v_div_fixup_f32 v83, v90, v83, v65
	v_div_scale_f32 v65, s[0:1], v82, v82, v114
	v_rcp_f32_e32 v90, v65
	s_nop 0
	v_fma_f32 v91, -v65, v90, 1.0
	v_fmac_f32_e32 v90, v91, v90
	v_div_scale_f32 v91, vcc, v114, v82, v114
	v_mul_f32_e32 v131, v91, v90
	v_fma_f32 v138, -v65, v131, v91
	v_fmac_f32_e32 v131, v138, v90
	v_fma_f32 v65, -v65, v131, v91
	v_div_fmas_f32 v65, v65, v90, v131
	v_div_fixup_f32 v82, v65, v82, v114
	v_mul_f32_e32 v65, 0xbfb8aa3b, v136
	v_exp_f32_e32 v131, v65
	s_nop 0
	v_pk_add_f32 v[90:91], v[130:131], 1.0 op_sel_hi:[1,0]
	s_nop 0
	v_div_scale_f32 v65, s[0:1], v91, v91, v136
	v_rcp_f32_e32 v114, v65
	s_nop 0
	v_fma_f32 v130, -v65, v114, 1.0
	v_fmac_f32_e32 v114, v130, v114
	v_div_scale_f32 v130, vcc, v136, v91, v136
	v_mul_f32_e32 v131, v130, v114
	v_fma_f32 v138, -v65, v131, v130
	v_fmac_f32_e32 v131, v138, v114
	v_fma_f32 v65, -v65, v131, v130
	v_div_fmas_f32 v65, v65, v114, v131
	v_div_fixup_f32 v91, v65, v91, v136
	v_div_scale_f32 v65, s[0:1], v90, v90, v137
	v_rcp_f32_e32 v114, v65
	s_mov_b32 s0, 0x358637bd
	v_fma_f32 v130, -v65, v114, 1.0
	v_fmac_f32_e32 v114, v130, v114
	v_div_scale_f32 v130, vcc, v137, v90, v137
	v_mul_f32_e32 v131, v130, v114
	v_fma_f32 v136, -v65, v131, v130
	v_fmac_f32_e32 v131, v136, v114
	v_fma_f32 v65, -v65, v131, v130
	v_div_fmas_f32 v65, v65, v114, v131
	v_div_fixup_f32 v90, v65, v90, v137
	v_lshlrev_b32_e32 v131, 16, v89
	v_lshlrev_b32_e32 v130, 16, v88
	v_lshlrev_b32_e32 v137, 16, v93
	v_lshlrev_b32_e32 v136, 16, v92
	v_pk_add_f32 v[130:131], v[130:131], v[136:137]
	v_and_b32_e32 v89, 0xffff0000, v89
	v_and_b32_e32 v88, 0xffff0000, v88
	v_and_b32_e32 v93, 0xffff0000, v93
	v_and_b32_e32 v92, 0xffff0000, v92
	v_pk_add_f32 v[88:89], v[88:89], v[92:93]
	v_pk_mul_f32 v[92:93], v[130:131], v[130:131]
	v_mov_b32_e32 v136, v0
	v_pk_fma_f32 v[92:93], v[88:89], v[88:89], v[92:93]
	v_mov_b32_e32 v137, v132
	v_mov_b32_e32 v132, v1
	v_pk_add_f32 v[0:1], v[136:137], v[132:133]
	v_mov_b32_e32 v132, v92
	v_mov_b32_e32 v133, v134
	v_pk_add_f32 v[0:1], v[132:133], v[0:1]
	v_mov_b32_e32 v134, v93
	v_pk_add_f32 v[0:1], v[134:135], v[0:1]
	ds_swizzle_b32 v93, v1 offset:swizzle(SWAP,1)
	ds_swizzle_b32 v92, v0 offset:swizzle(SWAP,1)
	s_waitcnt lgkmcnt(0)
	v_pk_add_f32 v[0:1], v[0:1], v[92:93]
	ds_swizzle_b32 v93, v1 offset:swizzle(SWAP,2)
	ds_swizzle_b32 v92, v0 offset:swizzle(SWAP,2)
	s_waitcnt lgkmcnt(0)
	v_pk_add_f32 v[0:1], v[0:1], v[92:93]
	ds_swizzle_b32 v93, v1 offset:swizzle(SWAP,4)
	ds_swizzle_b32 v92, v0 offset:swizzle(SWAP,4)
	s_waitcnt lgkmcnt(0)
	v_pk_add_f32 v[0:1], v[0:1], v[92:93]
	ds_swizzle_b32 v93, v1 offset:swizzle(SWAP,8)
	ds_swizzle_b32 v92, v0 offset:swizzle(SWAP,8)
	s_waitcnt lgkmcnt(0)
	v_pk_add_f32 v[0:1], v[0:1], v[92:93]
	ds_swizzle_b32 v93, v1 offset:swizzle(SWAP,16)
	ds_swizzle_b32 v92, v0 offset:swizzle(SWAP,16)
	s_waitcnt lgkmcnt(0)
	v_pk_add_f32 v[92:93], v[0:1], v[92:93]
	v_mov_b64_e32 v[0:1], s[0:1]
	v_pk_fma_f32 v[92:93], v[92:93], s[30:31], v[0:1] op_sel_hi:[1,0,0]
	s_nop 0
	v_mul_f32_e32 v65, 0x4b800000, v93
	v_cmp_gt_f32_e64 s[0:1], s47, v93
	v_cmp_gt_f32_e32 vcc, s47, v92
	s_nop 0
	v_cndmask_b32_e64 v65, v93, v65, s[0:1]
	v_rsq_f32_e32 v65, v65
	s_nop 0
	v_mul_f32_e32 v93, 0x45800000, v65
	v_cndmask_b32_e64 v114, v65, v93, s[0:1]
	v_pk_mul_f32 v[118:119], v[118:119], v[114:115] op_sel_hi:[1,0]
	v_pk_mul_f32 v[98:99], v[98:99], v[114:115] op_sel_hi:[1,0]
	v_pk_mul_f32 v[118:119], v[94:95], v[118:119]
	v_pk_mul_f32 v[98:99], v[10:11], v[98:99]
	v_pk_mul_f32 v[118:119], v[120:121], v[118:119]
	v_pk_mul_f32 v[120:121], v[124:125], v[114:115] op_sel_hi:[1,0]
	v_pk_mul_f32 v[98:99], v[122:123], v[98:99]
	v_pk_mul_f32 v[120:121], v[8:9], v[120:121]
	v_pk_mul_f32 v[96:97], v[96:97], v[114:115] op_sel_hi:[1,0]
	v_pk_mul_f32 v[100:101], v[100:101], v[120:121]
	v_pk_mul_f32 v[96:97], v[2:3], v[96:97]
	v_bfe_u32 v114, v99, 16, 1
	v_pk_mul_f32 v[96:97], v[128:129], v[96:97]
	v_add3_u32 v114, v99, v114, s48
	v_bfe_u32 v99, v101, 16, 1
	v_bfe_u32 v65, v97, 16, 1
	v_add3_u32 v99, v101, v99, s48
	v_add3_u32 v65, v97, v65, s48
	v_lshrrev_b32_e32 v99, 16, v99
	v_and_or_b32 v99, v65, s46, v99
	v_mul_f32_e32 v65, 0x4b800000, v92
	v_cndmask_b32_e32 v65, v92, v65, vcc
	v_rsq_f32_e32 v65, v65
	v_bfe_u32 v93, v96, 16, 1
	v_bfe_u32 v120, v98, 16, 1
	v_add3_u32 v120, v98, v120, s48
	v_add3_u32 v93, v96, v93, s48
	v_bfe_u32 v96, v118, 16, 1
	v_bfe_u32 v97, v119, 16, 1
	v_bfe_u32 v98, v100, 16, 1
	v_add3_u32 v98, v100, v98, s48
	v_add3_u32 v97, v119, v97, s48
	v_add3_u32 v96, v118, v96, s48
	v_mul_f32_e32 v92, 0x45800000, v65
	v_lshrrev_b32_e32 v96, 16, v96
	v_lshrrev_b32_e32 v97, 16, v97
	v_lshrrev_b32_e32 v98, 16, v98
	v_cndmask_b32_e32 v92, v65, v92, vcc
	v_and_or_b32 v98, v93, s46, v98
	v_and_or_b32 v97, v114, s46, v97
	v_and_or_b32 v96, v120, s46, v96
	v_pk_mul_f32 v[86:87], v[86:87], v[92:93] op_sel_hi:[1,0]
	global_store_dwordx4 v[116:117], v[96:99], off
	v_pk_mul_f32 v[86:87], v[10:11], v[86:87]
	v_lshlrev_b32_e32 v65, 16, v85
	v_pk_mul_f32 v[96:97], v[126:127], v[92:93] op_sel_hi:[1,0]
	v_lshlrev_b32_e32 v93, 16, v84
	v_pk_mul_f32 v[86:87], v[90:91], v[86:87]
	v_mul_f32_e32 v90, 0xbfb8aa3b, v93
	v_and_b32_e32 v98, 0xffff0000, v85
	v_mul_f32_e32 v85, 0xbfb8aa3b, v65
	v_exp_f32_e32 v90, v90
	v_exp_f32_e32 v91, v85
	v_and_b32_e32 v99, 0xffff0000, v84
	v_mul_f32_e32 v84, 0xbfb8aa3b, v99
	v_exp_f32_e32 v84, v84
	v_pk_add_f32 v[90:91], v[90:91], 1.0 op_sel_hi:[1,0]
	v_pk_mul_f32 v[96:97], v[94:95], v[96:97]
	v_div_scale_f32 v85, s[0:1], v91, v91, v65
	v_rcp_f32_e32 v100, v85
	v_pk_mul_f32 v[82:83], v[82:83], v[96:97]
	v_pk_mul_f32 v[96:97], v[130:131], v[92:93] op_sel_hi:[1,0]
	v_pk_mul_f32 v[88:89], v[88:89], v[92:93] op_sel_hi:[1,0]
	v_fma_f32 v101, -v85, v100, 1.0
	v_fmac_f32_e32 v100, v101, v100
	v_div_scale_f32 v101, vcc, v65, v91, v65
	v_mul_f32_e32 v114, v101, v100
	v_fma_f32 v118, -v85, v114, v101
	v_fmac_f32_e32 v114, v118, v100
	v_fma_f32 v85, -v85, v114, v101
	v_div_fmas_f32 v85, v85, v100, v114
	v_div_fixup_f32 v91, v85, v91, v65
	v_div_scale_f32 v65, s[0:1], v90, v90, v93
	v_rcp_f32_e32 v85, v65
	v_pk_mul_f32 v[96:97], v[8:9], v[96:97]
	v_pk_mul_f32 v[88:89], v[2:3], v[88:89]
	v_fma_f32 v100, -v65, v85, 1.0
	v_fmac_f32_e32 v85, v100, v85
	v_div_scale_f32 v100, vcc, v93, v90, v93
	v_mul_f32_e32 v101, v100, v85
	v_fma_f32 v114, -v65, v101, v100
	v_fmac_f32_e32 v101, v114, v85
	v_fma_f32 v65, -v65, v101, v100
	v_div_fmas_f32 v65, v65, v85, v101
	v_div_fixup_f32 v90, v65, v90, v93
	v_mul_f32_e32 v65, 0xbfb8aa3b, v98
	v_exp_f32_e32 v85, v65
	v_pk_mul_f32 v[90:91], v[90:91], v[96:97]
	v_pk_add_f32 v[84:85], v[84:85], 1.0 op_sel_hi:[1,0]
	s_nop 0
	v_div_scale_f32 v65, s[0:1], v85, v85, v98
	v_rcp_f32_e32 v92, v65
	s_nop 0
	v_fma_f32 v93, -v65, v92, 1.0
	v_fmac_f32_e32 v92, v93, v92
	v_div_scale_f32 v93, vcc, v98, v85, v98
	v_mul_f32_e32 v96, v93, v92
	v_fma_f32 v97, -v65, v96, v93
	v_fmac_f32_e32 v96, v97, v92
	v_fma_f32 v65, -v65, v96, v93
	v_div_fmas_f32 v65, v65, v92, v96
	v_div_fixup_f32 v85, v65, v85, v98
	v_div_scale_f32 v65, s[0:1], v84, v84, v99
	v_rcp_f32_e32 v92, v65
	s_nop 0
	v_fma_f32 v93, -v65, v92, 1.0
	v_fmac_f32_e32 v92, v93, v92
	v_div_scale_f32 v93, vcc, v99, v84, v99
	v_mul_f32_e32 v96, v93, v92
	v_fma_f32 v97, -v65, v96, v93
	v_fmac_f32_e32 v96, v97, v92
	v_fma_f32 v65, -v65, v96, v93
	v_div_fmas_f32 v65, v65, v92, v96
	v_div_fixup_f32 v84, v65, v84, v99
	v_pk_mul_f32 v[84:85], v[84:85], v[88:89]
	v_bfe_u32 v89, v87, 16, 1
	v_bfe_u32 v65, v85, 16, 1
	v_bfe_u32 v88, v84, 16, 1
	v_bfe_u32 v92, v86, 16, 1
	v_add3_u32 v86, v86, v92, s48
	v_add3_u32 v87, v87, v89, s48
	v_add3_u32 v84, v84, v88, s48
	v_add3_u32 v65, v85, v65, s48
	v_bfe_u32 v85, v82, 16, 1
	v_bfe_u32 v88, v83, 16, 1
	v_bfe_u32 v89, v90, 16, 1
	v_bfe_u32 v92, v91, 16, 1
	v_add3_u32 v91, v91, v92, s48
	v_add3_u32 v89, v90, v89, s48
	v_add3_u32 v83, v83, v88, s48
	v_add3_u32 v82, v82, v85, s48
	v_lshrrev_b32_e32 v82, 16, v82
	v_lshrrev_b32_e32 v83, 16, v83
	v_lshrrev_b32_e32 v88, 16, v89
	v_lshrrev_b32_e32 v85, 16, v91
	v_and_or_b32 v85, v65, s46, v85
	v_and_or_b32 v84, v84, s46, v88
	v_and_or_b32 v83, v87, s46, v83
	v_and_or_b32 v82, v86, s46, v82
	v_and_b32_e32 v89, 0xffff0000, v70
	global_store_dwordx4 v[116:117], v[82:85], off offset:1024
	v_lshlrev_b32_e32 v65, 16, v71
	v_lshlrev_b32_e32 v87, 16, v70
	v_lshlrev_b32_e32 v83, 16, v79
	v_lshlrev_b32_e32 v82, 16, v78
	v_lshlrev_b32_e32 v85, 16, v75
	v_lshlrev_b32_e32 v84, 16, v74
	v_mul_f32_e32 v70, 0xbfb8aa3b, v89
	v_pk_add_f32 v[82:83], v[82:83], v[84:85]
	v_mul_f32_e32 v84, 0xbfb8aa3b, v87
	v_exp_f32_e32 v86, v70
	v_mul_f32_e32 v70, 0xbfb8aa3b, v65
	v_exp_f32_e32 v84, v84
	v_exp_f32_e32 v85, v70
	v_and_b32_e32 v88, 0xffff0000, v71
	v_and_b32_e32 v93, 0xffff0000, v72
	v_and_b32_e32 v99, 0xffff0000, v56
	v_pk_add_f32 v[70:71], v[84:85], 1.0 op_sel_hi:[1,0]
	v_and_b32_e32 v79, 0xffff0000, v79
	v_div_scale_f32 v84, s[0:1], v71, v71, v65
	v_rcp_f32_e32 v85, v84
	v_and_b32_e32 v78, 0xffff0000, v78
	v_and_b32_e32 v75, 0xffff0000, v75
	v_and_b32_e32 v74, 0xffff0000, v74
	v_fma_f32 v90, -v84, v85, 1.0
	v_fmac_f32_e32 v85, v90, v85
	v_div_scale_f32 v90, vcc, v65, v71, v65
	v_mul_f32_e32 v91, v90, v85
	v_fma_f32 v92, -v84, v91, v90
	v_fmac_f32_e32 v91, v92, v85
	v_fma_f32 v84, -v84, v91, v90
	v_div_fmas_f32 v84, v84, v85, v91
	v_div_fixup_f32 v71, v84, v71, v65
	v_div_scale_f32 v65, s[0:1], v70, v70, v87
	v_rcp_f32_e32 v84, v65
	v_and_b32_e32 v92, 0xffff0000, v73
	v_pk_add_f32 v[74:75], v[78:79], v[74:75]
	v_pk_mul_f32 v[78:79], v[82:83], v[82:83]
	v_fma_f32 v85, -v65, v84, 1.0
	v_fmac_f32_e32 v84, v85, v84
	v_div_scale_f32 v85, vcc, v87, v70, v87
	v_mul_f32_e32 v90, v85, v84
	v_fma_f32 v91, -v65, v90, v85
	v_fmac_f32_e32 v90, v91, v84
	v_fma_f32 v65, -v65, v90, v85
	v_div_fmas_f32 v65, v65, v84, v90
	v_div_fixup_f32 v70, v65, v70, v87
	v_mul_f32_e32 v65, 0xbfb8aa3b, v88
	v_exp_f32_e32 v87, v65
	v_pk_fma_f32 v[78:79], v[74:75], v[74:75], v[78:79]
	v_pk_add_f32 v[84:85], v[86:87], 1.0 op_sel_hi:[1,0]
	s_nop 0
	v_div_scale_f32 v65, s[0:1], v85, v85, v88
	v_rcp_f32_e32 v86, v65
	s_nop 0
	v_fma_f32 v87, -v65, v86, 1.0
	v_fmac_f32_e32 v86, v87, v86
	v_div_scale_f32 v87, vcc, v88, v85, v88
	v_mul_f32_e32 v90, v87, v86
	v_fma_f32 v91, -v65, v90, v87
	v_fmac_f32_e32 v90, v91, v86
	v_fma_f32 v65, -v65, v90, v87
	v_div_fmas_f32 v65, v65, v86, v90
	v_div_fixup_f32 v85, v65, v85, v88
	v_div_scale_f32 v65, s[0:1], v84, v84, v89
	v_rcp_f32_e32 v86, v65
	v_lshlrev_b32_e32 v91, 16, v72
	v_mul_f32_e32 v72, 0xbfb8aa3b, v93
	v_fma_f32 v87, -v65, v86, 1.0
	v_fmac_f32_e32 v86, v87, v86
	v_div_scale_f32 v87, vcc, v89, v84, v89
	v_mul_f32_e32 v88, v87, v86
	v_fma_f32 v90, -v65, v88, v87
	v_fmac_f32_e32 v88, v90, v86
	v_fma_f32 v65, -v65, v88, v87
	v_div_fmas_f32 v65, v65, v86, v88
	v_div_fixup_f32 v84, v65, v84, v89
	v_lshlrev_b32_e32 v87, 16, v81
	v_lshlrev_b32_e32 v86, 16, v80
	v_lshlrev_b32_e32 v89, 16, v77
	v_lshlrev_b32_e32 v88, 16, v76
	v_lshlrev_b32_e32 v65, 16, v73
	v_pk_add_f32 v[86:87], v[86:87], v[88:89]
	v_mul_f32_e32 v88, 0xbfb8aa3b, v91
	v_exp_f32_e32 v90, v72
	v_mul_f32_e32 v72, 0xbfb8aa3b, v65
	v_exp_f32_e32 v88, v88
	v_exp_f32_e32 v89, v72
	v_and_b32_e32 v81, 0xffff0000, v81
	v_and_b32_e32 v80, 0xffff0000, v80
	v_and_b32_e32 v77, 0xffff0000, v77
	v_pk_add_f32 v[72:73], v[88:89], 1.0 op_sel_hi:[1,0]
	v_and_b32_e32 v76, 0xffff0000, v76
	v_div_scale_f32 v88, s[0:1], v73, v73, v65
	v_rcp_f32_e32 v89, v88
	v_pk_add_f32 v[76:77], v[80:81], v[76:77]
	v_pk_mul_f32 v[80:81], v[86:87], v[86:87]
	v_fma_f32 v96, -v88, v89, 1.0
	v_fmac_f32_e32 v89, v96, v89
	v_div_scale_f32 v96, vcc, v65, v73, v65
	v_mul_f32_e32 v97, v96, v89
	v_fma_f32 v98, -v88, v97, v96
	v_fmac_f32_e32 v97, v98, v89
	v_fma_f32 v88, -v88, v97, v96
	v_div_fmas_f32 v88, v88, v89, v97
	v_div_fixup_f32 v73, v88, v73, v65
	v_div_scale_f32 v65, s[0:1], v72, v72, v91
	v_rcp_f32_e32 v88, v65
	v_and_b32_e32 v98, 0xffff0000, v57
	v_pk_fma_f32 v[80:81], v[76:77], v[76:77], v[80:81]
	v_fma_f32 v89, -v65, v88, 1.0
	v_fmac_f32_e32 v88, v89, v88
	v_div_scale_f32 v89, vcc, v91, v72, v91
	v_mul_f32_e32 v96, v89, v88
	v_fma_f32 v97, -v65, v96, v89
	v_fmac_f32_e32 v96, v97, v88
	v_fma_f32 v65, -v65, v96, v89
	v_div_fmas_f32 v65, v65, v88, v96
	v_div_fixup_f32 v72, v65, v72, v91
	v_mul_f32_e32 v65, 0xbfb8aa3b, v92
	v_exp_f32_e32 v91, v65
	s_nop 0
	v_pk_add_f32 v[88:89], v[90:91], 1.0 op_sel_hi:[1,0]
	s_nop 0
	v_div_scale_f32 v65, s[0:1], v89, v89, v92
	v_rcp_f32_e32 v90, v65
	s_nop 0
	v_fma_f32 v91, -v65, v90, 1.0
	v_fmac_f32_e32 v90, v91, v90
	v_div_scale_f32 v91, vcc, v92, v89, v92
	v_mul_f32_e32 v96, v91, v90
	v_fma_f32 v97, -v65, v96, v91
	v_fmac_f32_e32 v96, v97, v90
	v_fma_f32 v65, -v65, v96, v91
	v_div_fmas_f32 v65, v65, v90, v96
	v_div_fixup_f32 v89, v65, v89, v92
	v_div_scale_f32 v65, s[0:1], v88, v88, v93
	v_rcp_f32_e32 v90, v65
	v_lshlrev_b32_e32 v97, 16, v56
	v_mul_f32_e32 v56, 0xbfb8aa3b, v99
	v_fma_f32 v91, -v65, v90, 1.0
	v_fmac_f32_e32 v90, v91, v90
	v_div_scale_f32 v91, vcc, v93, v88, v93
	v_mul_f32_e32 v92, v91, v90
	v_fma_f32 v96, -v65, v92, v91
	v_fmac_f32_e32 v92, v96, v90
	v_fma_f32 v65, -v65, v92, v91
	v_div_fmas_f32 v65, v65, v90, v92
	v_div_fixup_f32 v88, v65, v88, v93
	v_lshlrev_b32_e32 v91, 16, v67
	v_lshlrev_b32_e32 v90, 16, v66
	v_lshlrev_b32_e32 v93, 16, v61
	v_lshlrev_b32_e32 v92, 16, v60
	v_pk_add_f32 v[90:91], v[90:91], v[92:93]
	v_and_b32_e32 v67, 0xffff0000, v67
	v_and_b32_e32 v66, 0xffff0000, v66
	v_and_b32_e32 v61, 0xffff0000, v61
	v_and_b32_e32 v60, 0xffff0000, v60
	v_pk_add_f32 v[60:61], v[66:67], v[60:61]
	v_pk_mul_f32 v[66:67], v[90:91], v[90:91]
	v_lshlrev_b32_e32 v65, 16, v57
	v_pk_fma_f32 v[92:93], v[60:61], v[60:61], v[66:67]
	v_mul_f32_e32 v66, 0xbfb8aa3b, v97
	v_exp_f32_e32 v96, v56
	v_mul_f32_e32 v56, 0xbfb8aa3b, v65
	v_exp_f32_e32 v66, v66
	v_exp_f32_e32 v67, v56
	s_nop 0
	v_pk_add_f32 v[56:57], v[66:67], 1.0 op_sel_hi:[1,0]
	s_nop 0
	v_div_scale_f32 v66, s[0:1], v57, v57, v65
	v_rcp_f32_e32 v67, v66
	s_nop 0
	v_fma_f32 v100, -v66, v67, 1.0
	v_fmac_f32_e32 v67, v100, v67
	v_div_scale_f32 v100, vcc, v65, v57, v65
	v_mul_f32_e32 v101, v100, v67
	v_fma_f32 v114, -v66, v101, v100
	v_fmac_f32_e32 v101, v114, v67
	v_fma_f32 v66, -v66, v101, v100
	v_div_fmas_f32 v66, v66, v67, v101
	v_div_fixup_f32 v57, v66, v57, v65
	v_div_scale_f32 v65, s[0:1], v56, v56, v97
	v_rcp_f32_e32 v66, v65
	s_nop 0
	v_fma_f32 v67, -v65, v66, 1.0
	v_fmac_f32_e32 v66, v67, v66
	v_div_scale_f32 v67, vcc, v97, v56, v97
	v_mul_f32_e32 v100, v67, v66
	v_fma_f32 v101, -v65, v100, v67
	v_fmac_f32_e32 v100, v101, v66
	v_fma_f32 v65, -v65, v100, v67
	v_div_fmas_f32 v65, v65, v66, v100
	v_div_fixup_f32 v56, v65, v56, v97
	v_mul_f32_e32 v65, 0xbfb8aa3b, v98
	v_exp_f32_e32 v97, v65
	s_nop 0
	v_pk_add_f32 v[66:67], v[96:97], 1.0 op_sel_hi:[1,0]
	s_nop 0
	v_div_scale_f32 v65, s[0:1], v67, v67, v98
	v_rcp_f32_e32 v96, v65
	s_nop 0
	v_fma_f32 v97, -v65, v96, 1.0
	v_fmac_f32_e32 v96, v97, v96
	v_div_scale_f32 v97, vcc, v98, v67, v98
	v_mul_f32_e32 v100, v97, v96
	v_fma_f32 v101, -v65, v100, v97
	v_fmac_f32_e32 v100, v101, v96
	v_fma_f32 v65, -v65, v100, v97
	v_div_fmas_f32 v65, v65, v96, v100
	v_div_fixup_f32 v67, v65, v67, v98
	v_div_scale_f32 v65, s[0:1], v66, v66, v99
	v_rcp_f32_e32 v96, v65
	s_nop 0
	v_fma_f32 v97, -v65, v96, 1.0
	v_fmac_f32_e32 v96, v97, v96
	v_div_scale_f32 v97, vcc, v99, v66, v99
	v_mul_f32_e32 v98, v97, v96
	v_fma_f32 v100, -v65, v98, v97
	v_fmac_f32_e32 v98, v100, v96
	v_fma_f32 v65, -v65, v98, v97
	v_div_fmas_f32 v65, v65, v96, v98
	v_div_fixup_f32 v66, v65, v66, v99
	v_lshlrev_b32_e32 v97, 16, v69
	v_lshlrev_b32_e32 v96, 16, v68
	v_lshlrev_b32_e32 v99, 16, v63
	v_lshlrev_b32_e32 v98, 16, v62
	v_pk_add_f32 v[96:97], v[96:97], v[98:99]
	v_and_b32_e32 v69, 0xffff0000, v69
	v_and_b32_e32 v68, 0xffff0000, v68
	v_and_b32_e32 v63, 0xffff0000, v63
	v_and_b32_e32 v62, 0xffff0000, v62
	v_pk_add_f32 v[62:63], v[68:69], v[62:63]
	v_pk_mul_f32 v[68:69], v[96:97], v[96:97]
	v_mov_b32_e32 v98, v92
	v_pk_fma_f32 v[68:69], v[62:63], v[62:63], v[68:69]
	v_mov_b32_e32 v99, v78
	v_mov_b32_e32 v78, v93
	v_pk_add_f32 v[78:79], v[98:99], v[78:79]
	v_mov_b32_e32 v92, v68
	v_mov_b32_e32 v93, v80
	v_pk_add_f32 v[78:79], v[92:93], v[78:79]
	v_mov_b32_e32 v80, v69
	v_pk_add_f32 v[68:69], v[80:81], v[78:79]
	ds_swizzle_b32 v79, v69 offset:swizzle(SWAP,1)
	ds_swizzle_b32 v78, v68 offset:swizzle(SWAP,1)
	s_waitcnt lgkmcnt(0)
	v_pk_add_f32 v[68:69], v[68:69], v[78:79]
	ds_swizzle_b32 v79, v69 offset:swizzle(SWAP,2)
	ds_swizzle_b32 v78, v68 offset:swizzle(SWAP,2)
	s_waitcnt lgkmcnt(0)
	v_pk_add_f32 v[68:69], v[68:69], v[78:79]
	ds_swizzle_b32 v79, v69 offset:swizzle(SWAP,4)
	ds_swizzle_b32 v78, v68 offset:swizzle(SWAP,4)
	s_waitcnt lgkmcnt(0)
	v_pk_add_f32 v[68:69], v[68:69], v[78:79]
	ds_swizzle_b32 v79, v69 offset:swizzle(SWAP,8)
	ds_swizzle_b32 v78, v68 offset:swizzle(SWAP,8)
	s_waitcnt lgkmcnt(0)
	v_pk_add_f32 v[68:69], v[68:69], v[78:79]
	ds_swizzle_b32 v79, v69 offset:swizzle(SWAP,16)
	ds_swizzle_b32 v78, v68 offset:swizzle(SWAP,16)
	s_waitcnt lgkmcnt(0)
	v_pk_add_f32 v[68:69], v[68:69], v[78:79]
	s_nop 0
	v_pk_fma_f32 v[78:79], v[68:69], s[30:31], v[0:1] op_sel_hi:[1,0,0]
	s_nop 0
	v_mul_f32_e32 v65, 0x4b800000, v79
	v_cmp_gt_f32_e64 s[0:1], s47, v79
	v_cmp_gt_f32_e32 vcc, s47, v78
	s_nop 0
	v_cndmask_b32_e64 v65, v79, v65, s[0:1]
	v_rsq_f32_e32 v65, v65
	s_nop 0
	v_mul_f32_e32 v68, 0x45800000, v65
	v_cndmask_b32_e64 v68, v65, v68, s[0:1]
	v_pk_mul_f32 v[80:81], v[82:83], v[68:69] op_sel_hi:[1,0]
	v_pk_mul_f32 v[74:75], v[74:75], v[68:69] op_sel_hi:[1,0]
	v_pk_mul_f32 v[80:81], v[94:95], v[80:81]
	v_pk_mul_f32 v[74:75], v[10:11], v[74:75]
	v_pk_mul_f32 v[70:71], v[70:71], v[80:81]
	v_pk_mul_f32 v[80:81], v[86:87], v[68:69] op_sel_hi:[1,0]
	v_pk_mul_f32 v[68:69], v[76:77], v[68:69] op_sel_hi:[1,0]
	v_pk_mul_f32 v[74:75], v[84:85], v[74:75]
	v_pk_mul_f32 v[68:69], v[2:3], v[68:69]
	v_pk_mul_f32 v[80:81], v[8:9], v[80:81]
	v_pk_mul_f32 v[68:69], v[88:89], v[68:69]
	v_pk_mul_f32 v[72:73], v[72:73], v[80:81]
	v_bfe_u32 v65, v69, 16, 1
	v_bfe_u32 v76, v68, 16, 1
	v_bfe_u32 v79, v74, 16, 1
	v_add3_u32 v74, v74, v79, s48
	v_add3_u32 v68, v68, v76, s48
	v_add3_u32 v65, v69, v65, s48
	v_bfe_u32 v69, v70, 16, 1
	v_bfe_u32 v76, v71, 16, 1
	v_bfe_u32 v79, v73, 16, 1
	v_add3_u32 v73, v73, v79, s48
	v_add3_u32 v71, v71, v76, s48
	v_add3_u32 v69, v70, v69, s48
	v_lshrrev_b32_e32 v76, 16, v69
	v_lshrrev_b32_e32 v69, 16, v71
	v_lshrrev_b32_e32 v71, 16, v73
	v_and_or_b32 v71, v65, s46, v71
	v_mul_f32_e32 v65, 0x4b800000, v78
	v_bfe_u32 v77, v75, 16, 1
	v_cndmask_b32_e32 v65, v78, v65, vcc
	v_add3_u32 v75, v75, v77, s48
	v_bfe_u32 v77, v72, 16, 1
	v_rsq_f32_e32 v65, v65
	v_add3_u32 v72, v72, v77, s48
	v_lshrrev_b32_e32 v70, 16, v72
	v_and_or_b32 v70, v68, s46, v70
	v_and_or_b32 v69, v75, s46, v69
	v_and_or_b32 v68, v74, s46, v76
	global_store_dwordx4 v[116:117], v[68:71], off offset:2048
	v_and_b32_e32 v72, 0xffff0000, v59
	v_and_b32_e32 v73, 0xffff0000, v58
	v_mul_f32_e32 v68, 0x45800000, v65
	v_cndmask_b32_e32 v68, v65, v68, vcc
	v_pk_mul_f32 v[60:61], v[60:61], v[68:69] op_sel_hi:[1,0]
	v_pk_mul_f32 v[70:71], v[90:91], v[68:69] op_sel_hi:[1,0]
	v_pk_mul_f32 v[60:61], v[10:11], v[60:61]
	v_lshlrev_b32_e32 v65, 16, v59
	v_lshlrev_b32_e32 v69, 16, v58
	v_pk_mul_f32 v[60:61], v[66:67], v[60:61]
	v_mul_f32_e32 v66, 0xbfb8aa3b, v69
	v_mul_f32_e32 v59, 0xbfb8aa3b, v65
	v_exp_f32_e32 v66, v66
	v_exp_f32_e32 v67, v59
	v_mul_f32_e32 v58, 0xbfb8aa3b, v73
	v_exp_f32_e32 v58, v58
	v_pk_mul_f32 v[70:71], v[94:95], v[70:71]
	v_pk_add_f32 v[66:67], v[66:67], 1.0 op_sel_hi:[1,0]
	v_pk_mul_f32 v[56:57], v[56:57], v[70:71]
	v_div_scale_f32 v59, s[0:1], v67, v67, v65
	v_rcp_f32_e32 v74, v59
	v_pk_mul_f32 v[70:71], v[96:97], v[68:69] op_sel_hi:[1,0]
	v_pk_mul_f32 v[62:63], v[62:63], v[68:69] op_sel_hi:[1,0]
	v_pk_mul_f32 v[70:71], v[8:9], v[70:71]
	v_fma_f32 v75, -v59, v74, 1.0
	v_fmac_f32_e32 v74, v75, v74
	v_div_scale_f32 v75, vcc, v65, v67, v65
	v_mul_f32_e32 v76, v75, v74
	v_fma_f32 v77, -v59, v76, v75
	v_fmac_f32_e32 v76, v77, v74
	v_fma_f32 v59, -v59, v76, v75
	v_div_fmas_f32 v59, v59, v74, v76
	v_div_fixup_f32 v67, v59, v67, v65
	v_div_scale_f32 v59, s[0:1], v66, v66, v69
	v_rcp_f32_e32 v65, v59
	v_pk_mul_f32 v[62:63], v[2:3], v[62:63]
	v_fma_f32 v74, -v59, v65, 1.0
	v_fmac_f32_e32 v65, v74, v65
	v_div_scale_f32 v74, vcc, v69, v66, v69
	v_mul_f32_e32 v75, v74, v65
	v_fma_f32 v76, -v59, v75, v74
	v_fmac_f32_e32 v75, v76, v65
	v_fma_f32 v59, -v59, v75, v74
	v_div_fmas_f32 v59, v59, v65, v75
	v_div_fixup_f32 v66, v59, v66, v69
	v_mul_f32_e32 v59, 0xbfb8aa3b, v72
	v_exp_f32_e32 v59, v59
	v_pk_mul_f32 v[66:67], v[66:67], v[70:71]
	v_pk_add_f32 v[58:59], v[58:59], 1.0 op_sel_hi:[1,0]
	s_nop 0
	v_div_scale_f32 v65, s[0:1], v59, v59, v72
	v_rcp_f32_e32 v68, v65
	s_nop 0
	v_fma_f32 v69, -v65, v68, 1.0
	v_fmac_f32_e32 v68, v69, v68
	v_div_scale_f32 v69, vcc, v72, v59, v72
	v_mul_f32_e32 v70, v69, v68
	v_fma_f32 v71, -v65, v70, v69
	v_fmac_f32_e32 v70, v71, v68
	v_fma_f32 v65, -v65, v70, v69
	v_div_fmas_f32 v65, v65, v68, v70
	v_div_fixup_f32 v59, v65, v59, v72
	v_div_scale_f32 v65, s[0:1], v58, v58, v73
	v_rcp_f32_e32 v68, v65
	s_nop 0
	v_fma_f32 v69, -v65, v68, 1.0
	v_fmac_f32_e32 v68, v69, v68
	v_div_scale_f32 v69, vcc, v73, v58, v73
	v_mul_f32_e32 v70, v69, v68
	v_fma_f32 v71, -v65, v70, v69
	v_fmac_f32_e32 v70, v71, v68
	v_fma_f32 v65, -v65, v70, v69
	v_div_fmas_f32 v65, v65, v68, v70
	v_div_fixup_f32 v58, v65, v58, v73
	v_pk_mul_f32 v[58:59], v[58:59], v[62:63]
	v_bfe_u32 v65, v61, 16, 1
	v_bfe_u32 v62, v59, 16, 1
	v_bfe_u32 v63, v58, 16, 1
	v_bfe_u32 v68, v60, 16, 1
	v_add3_u32 v60, v60, v68, s48
	v_add3_u32 v61, v61, v65, s48
	v_add3_u32 v58, v58, v63, s48
	v_add3_u32 v59, v59, v62, s48
	v_bfe_u32 v62, v56, 16, 1
	v_bfe_u32 v63, v57, 16, 1
	v_bfe_u32 v65, v66, 16, 1
	v_bfe_u32 v68, v67, 16, 1
	v_add3_u32 v67, v67, v68, s48
	v_add3_u32 v65, v66, v65, s48
	v_add3_u32 v57, v57, v63, s48
	v_add3_u32 v56, v56, v62, s48
	v_lshrrev_b32_e32 v56, 16, v56
	v_lshrrev_b32_e32 v57, 16, v57
	v_lshrrev_b32_e32 v62, 16, v65
	v_lshrrev_b32_e32 v63, 16, v67
	v_and_or_b32 v59, v59, s46, v63
	v_and_or_b32 v58, v58, s46, v62
	v_and_or_b32 v57, v61, s46, v57
	v_and_or_b32 v56, v60, s46, v56
	v_and_b32_e32 v65, 0xffff0000, v44
	global_store_dwordx4 v[116:117], v[56:59], off offset:3072
	v_lshlrev_b32_e32 v61, 16, v45
	v_lshlrev_b32_e32 v62, 16, v44
	v_lshlrev_b32_e32 v57, 16, v49
	v_lshlrev_b32_e32 v56, 16, v48
	v_lshlrev_b32_e32 v59, 16, v53
	v_lshlrev_b32_e32 v58, 16, v52
	v_mul_f32_e32 v44, 0xbfb8aa3b, v65
	v_pk_add_f32 v[56:57], v[56:57], v[58:59]
	v_mul_f32_e32 v58, 0xbfb8aa3b, v62
	v_exp_f32_e32 v60, v44
	v_mul_f32_e32 v44, 0xbfb8aa3b, v61
	v_exp_f32_e32 v58, v58
	v_exp_f32_e32 v59, v44
	v_and_b32_e32 v63, 0xffff0000, v45
	v_and_b32_e32 v69, 0xffff0000, v46
	v_and_b32_e32 v73, 0xffff0000, v32
	v_pk_add_f32 v[44:45], v[58:59], 1.0 op_sel_hi:[1,0]
	v_and_b32_e32 v49, 0xffff0000, v49
	v_div_scale_f32 v58, s[0:1], v45, v45, v61
	v_rcp_f32_e32 v59, v58
	v_and_b32_e32 v48, 0xffff0000, v48
	v_and_b32_e32 v53, 0xffff0000, v53
	v_and_b32_e32 v52, 0xffff0000, v52
	v_fma_f32 v66, -v58, v59, 1.0
	v_fmac_f32_e32 v59, v66, v59
	v_div_scale_f32 v66, vcc, v61, v45, v61
	v_mul_f32_e32 v67, v66, v59
	v_fma_f32 v68, -v58, v67, v66
	v_fmac_f32_e32 v67, v68, v59
	v_fma_f32 v58, -v58, v67, v66
	v_div_fmas_f32 v58, v58, v59, v67
	v_div_fixup_f32 v45, v58, v45, v61
	v_div_scale_f32 v58, s[0:1], v44, v44, v62
	v_rcp_f32_e32 v59, v58
	v_and_b32_e32 v68, 0xffff0000, v47
	v_pk_add_f32 v[48:49], v[48:49], v[52:53]
	v_pk_mul_f32 v[52:53], v[56:57], v[56:57]
	v_fma_f32 v61, -v58, v59, 1.0
	v_fmac_f32_e32 v59, v61, v59
	v_div_scale_f32 v61, vcc, v62, v44, v62
	v_mul_f32_e32 v66, v61, v59
	v_fma_f32 v67, -v58, v66, v61
	v_fmac_f32_e32 v66, v67, v59
	v_fma_f32 v58, -v58, v66, v61
	v_div_fmas_f32 v58, v58, v59, v66
	v_div_fixup_f32 v44, v58, v44, v62
	v_mul_f32_e32 v58, 0xbfb8aa3b, v63
	v_exp_f32_e32 v61, v58
	v_pk_fma_f32 v[52:53], v[48:49], v[48:49], v[52:53]
	v_pk_add_f32 v[58:59], v[60:61], 1.0 op_sel_hi:[1,0]
	s_nop 0
	v_div_scale_f32 v60, s[0:1], v59, v59, v63
	v_rcp_f32_e32 v61, v60
	s_nop 0
	v_fma_f32 v62, -v60, v61, 1.0
	v_fmac_f32_e32 v61, v62, v61
	v_div_scale_f32 v62, vcc, v63, v59, v63
	v_mul_f32_e32 v66, v62, v61
	v_fma_f32 v67, -v60, v66, v62
	v_fmac_f32_e32 v66, v67, v61
	v_fma_f32 v60, -v60, v66, v62
	v_div_fmas_f32 v60, v60, v61, v66
	v_div_fixup_f32 v59, v60, v59, v63
	v_div_scale_f32 v60, s[0:1], v58, v58, v65
	v_rcp_f32_e32 v61, v60
	v_lshlrev_b32_e32 v67, 16, v46
	v_mul_f32_e32 v46, 0xbfb8aa3b, v69
	v_fma_f32 v62, -v60, v61, 1.0
	v_fmac_f32_e32 v61, v62, v61
	v_div_scale_f32 v62, vcc, v65, v58, v65
	v_mul_f32_e32 v63, v62, v61
	v_fma_f32 v66, -v60, v63, v62
	v_fmac_f32_e32 v63, v66, v61
	v_fma_f32 v60, -v60, v63, v62
	v_div_fmas_f32 v60, v60, v61, v63
	v_div_fixup_f32 v58, v60, v58, v65
	v_lshlrev_b32_e32 v61, 16, v51
	v_lshlrev_b32_e32 v60, 16, v50
	v_lshlrev_b32_e32 v63, 16, v55
	v_lshlrev_b32_e32 v62, 16, v54
	v_lshlrev_b32_e32 v65, 16, v47
	v_pk_add_f32 v[60:61], v[60:61], v[62:63]
	v_mul_f32_e32 v62, 0xbfb8aa3b, v67
	v_exp_f32_e32 v66, v46
	v_mul_f32_e32 v46, 0xbfb8aa3b, v65
	v_exp_f32_e32 v62, v62
	v_exp_f32_e32 v63, v46
	v_and_b32_e32 v51, 0xffff0000, v51
	v_and_b32_e32 v50, 0xffff0000, v50
	v_and_b32_e32 v55, 0xffff0000, v55
	v_pk_add_f32 v[46:47], v[62:63], 1.0 op_sel_hi:[1,0]
	v_and_b32_e32 v54, 0xffff0000, v54
	v_div_scale_f32 v62, s[0:1], v47, v47, v65
	v_rcp_f32_e32 v63, v62
	v_pk_add_f32 v[50:51], v[50:51], v[54:55]
	v_pk_mul_f32 v[54:55], v[60:61], v[60:61]
	v_fma_f32 v70, -v62, v63, 1.0
	v_fmac_f32_e32 v63, v70, v63
	v_div_scale_f32 v70, vcc, v65, v47, v65
	v_mul_f32_e32 v71, v70, v63
	v_fma_f32 v72, -v62, v71, v70
	v_fmac_f32_e32 v71, v72, v63
	v_fma_f32 v62, -v62, v71, v70
	v_div_fmas_f32 v62, v62, v63, v71
	v_div_fixup_f32 v47, v62, v47, v65
	v_div_scale_f32 v62, s[0:1], v46, v46, v67
	v_rcp_f32_e32 v63, v62
	v_and_b32_e32 v72, 0xffff0000, v33
	v_pk_fma_f32 v[54:55], v[50:51], v[50:51], v[54:55]
	v_fma_f32 v65, -v62, v63, 1.0
	v_fmac_f32_e32 v63, v65, v63
	v_div_scale_f32 v65, vcc, v67, v46, v67
	v_mul_f32_e32 v70, v65, v63
	v_fma_f32 v71, -v62, v70, v65
	v_fmac_f32_e32 v70, v71, v63
	v_fma_f32 v62, -v62, v70, v65
	v_div_fmas_f32 v62, v62, v63, v70
	v_div_fixup_f32 v46, v62, v46, v67
	v_mul_f32_e32 v62, 0xbfb8aa3b, v68
	v_exp_f32_e32 v67, v62
	s_nop 0
	v_pk_add_f32 v[62:63], v[66:67], 1.0 op_sel_hi:[1,0]
	s_nop 0
	v_div_scale_f32 v65, s[0:1], v63, v63, v68
	v_rcp_f32_e32 v66, v65
	s_nop 0
	v_fma_f32 v67, -v65, v66, 1.0
	v_fmac_f32_e32 v66, v67, v66
	v_div_scale_f32 v67, vcc, v68, v63, v68
	v_mul_f32_e32 v70, v67, v66
	v_fma_f32 v71, -v65, v70, v67
	v_fmac_f32_e32 v70, v71, v66
	v_fma_f32 v65, -v65, v70, v67
	v_div_fmas_f32 v65, v65, v66, v70
	v_div_fixup_f32 v63, v65, v63, v68
	v_div_scale_f32 v65, s[0:1], v62, v62, v69
	v_rcp_f32_e32 v66, v65
	v_lshlrev_b32_e32 v71, 16, v32
	v_mul_f32_e32 v32, 0xbfb8aa3b, v73
	v_fma_f32 v67, -v65, v66, 1.0
	v_fmac_f32_e32 v66, v67, v66
	v_div_scale_f32 v67, vcc, v69, v62, v69
	v_mul_f32_e32 v68, v67, v66
	v_fma_f32 v70, -v65, v68, v67
	v_fmac_f32_e32 v68, v70, v66
	v_fma_f32 v65, -v65, v68, v67
	v_div_fmas_f32 v65, v65, v66, v68
	v_div_fixup_f32 v62, v65, v62, v69
	v_lshlrev_b32_e32 v67, 16, v41
	v_lshlrev_b32_e32 v66, 16, v40
	v_lshlrev_b32_e32 v69, 16, v37
	v_lshlrev_b32_e32 v68, 16, v36
	v_pk_add_f32 v[66:67], v[66:67], v[68:69]
	v_and_b32_e32 v41, 0xffff0000, v41
	v_and_b32_e32 v40, 0xffff0000, v40
	v_and_b32_e32 v37, 0xffff0000, v37
	v_and_b32_e32 v36, 0xffff0000, v36
	v_pk_add_f32 v[36:37], v[40:41], v[36:37]
	v_pk_mul_f32 v[40:41], v[66:67], v[66:67]
	v_lshlrev_b32_e32 v65, 16, v33
	v_pk_fma_f32 v[68:69], v[36:37], v[36:37], v[40:41]
	v_mul_f32_e32 v40, 0xbfb8aa3b, v71
	v_exp_f32_e32 v70, v32
	v_mul_f32_e32 v32, 0xbfb8aa3b, v65
	v_exp_f32_e32 v40, v40
	v_exp_f32_e32 v41, v32
	s_nop 0
	v_pk_add_f32 v[32:33], v[40:41], 1.0 op_sel_hi:[1,0]
	s_nop 0
	v_div_scale_f32 v40, s[0:1], v33, v33, v65
	v_rcp_f32_e32 v41, v40
	s_nop 0
	v_fma_f32 v74, -v40, v41, 1.0
	v_fmac_f32_e32 v41, v74, v41
	v_div_scale_f32 v74, vcc, v65, v33, v65
	v_mul_f32_e32 v75, v74, v41
	v_fma_f32 v76, -v40, v75, v74
	v_fmac_f32_e32 v75, v76, v41
	v_fma_f32 v40, -v40, v75, v74
	v_div_fmas_f32 v40, v40, v41, v75
	v_div_fixup_f32 v33, v40, v33, v65
	v_div_scale_f32 v40, s[0:1], v32, v32, v71
	v_rcp_f32_e32 v41, v40
	s_nop 0
	v_fma_f32 v65, -v40, v41, 1.0
	v_fmac_f32_e32 v41, v65, v41
	v_div_scale_f32 v65, vcc, v71, v32, v71
	v_mul_f32_e32 v74, v65, v41
	v_fma_f32 v75, -v40, v74, v65
	v_fmac_f32_e32 v74, v75, v41
	v_fma_f32 v40, -v40, v74, v65
	v_div_fmas_f32 v40, v40, v41, v74
	v_div_fixup_f32 v32, v40, v32, v71
	v_mul_f32_e32 v40, 0xbfb8aa3b, v72
	v_exp_f32_e32 v71, v40
	s_nop 0
	v_pk_add_f32 v[40:41], v[70:71], 1.0 op_sel_hi:[1,0]
	s_nop 0
	v_div_scale_f32 v65, s[0:1], v41, v41, v72
	v_rcp_f32_e32 v70, v65
	s_nop 0
	v_fma_f32 v71, -v65, v70, 1.0
	v_fmac_f32_e32 v70, v71, v70
	v_div_scale_f32 v71, vcc, v72, v41, v72
	v_mul_f32_e32 v74, v71, v70
	v_fma_f32 v75, -v65, v74, v71
	v_fmac_f32_e32 v74, v75, v70
	v_fma_f32 v65, -v65, v74, v71
	v_div_fmas_f32 v65, v65, v70, v74
	v_div_fixup_f32 v41, v65, v41, v72
	v_div_scale_f32 v65, s[0:1], v40, v40, v73
	v_rcp_f32_e32 v70, v65
	s_nop 0
	v_fma_f32 v71, -v65, v70, 1.0
	v_fmac_f32_e32 v70, v71, v70
	v_div_scale_f32 v71, vcc, v73, v40, v73
	v_mul_f32_e32 v72, v71, v70
	v_fma_f32 v74, -v65, v72, v71
	v_fmac_f32_e32 v72, v74, v70
	v_fma_f32 v65, -v65, v72, v71
	v_div_fmas_f32 v65, v65, v70, v72
	v_div_fixup_f32 v40, v65, v40, v73
	v_lshlrev_b32_e32 v71, 16, v43
	v_lshlrev_b32_e32 v70, 16, v42
	v_lshlrev_b32_e32 v73, 16, v39
	v_lshlrev_b32_e32 v72, 16, v38
	v_pk_add_f32 v[70:71], v[70:71], v[72:73]
	v_and_b32_e32 v43, 0xffff0000, v43
	v_and_b32_e32 v42, 0xffff0000, v42
	v_and_b32_e32 v39, 0xffff0000, v39
	v_and_b32_e32 v38, 0xffff0000, v38
	v_pk_add_f32 v[38:39], v[42:43], v[38:39]
	v_pk_mul_f32 v[42:43], v[70:71], v[70:71]
	v_mov_b32_e32 v72, v68
	v_pk_fma_f32 v[42:43], v[38:39], v[38:39], v[42:43]
	v_mov_b32_e32 v73, v52
	v_mov_b32_e32 v52, v69
	v_pk_add_f32 v[52:53], v[72:73], v[52:53]
	v_mov_b32_e32 v68, v42
	v_mov_b32_e32 v69, v54
	v_pk_add_f32 v[52:53], v[68:69], v[52:53]
	v_mov_b32_e32 v54, v43
	v_pk_add_f32 v[42:43], v[54:55], v[52:53]
	ds_swizzle_b32 v53, v43 offset:swizzle(SWAP,1)
	ds_swizzle_b32 v52, v42 offset:swizzle(SWAP,1)
	s_waitcnt lgkmcnt(0)
	v_pk_add_f32 v[42:43], v[42:43], v[52:53]
	ds_swizzle_b32 v53, v43 offset:swizzle(SWAP,2)
	ds_swizzle_b32 v52, v42 offset:swizzle(SWAP,2)
	s_waitcnt lgkmcnt(0)
	v_pk_add_f32 v[42:43], v[42:43], v[52:53]
	ds_swizzle_b32 v53, v43 offset:swizzle(SWAP,4)
	ds_swizzle_b32 v52, v42 offset:swizzle(SWAP,4)
	s_waitcnt lgkmcnt(0)
	v_pk_add_f32 v[42:43], v[42:43], v[52:53]
	ds_swizzle_b32 v53, v43 offset:swizzle(SWAP,8)
	ds_swizzle_b32 v52, v42 offset:swizzle(SWAP,8)
	s_waitcnt lgkmcnt(0)
	v_pk_add_f32 v[42:43], v[42:43], v[52:53]
	ds_swizzle_b32 v53, v43 offset:swizzle(SWAP,16)
	ds_swizzle_b32 v52, v42 offset:swizzle(SWAP,16)
	s_waitcnt lgkmcnt(0)
	v_pk_add_f32 v[42:43], v[42:43], v[52:53]
	s_nop 0
	v_pk_fma_f32 v[52:53], v[42:43], s[30:31], v[0:1] op_sel_hi:[1,0,0]
	s_nop 0
	v_mul_f32_e32 v42, 0x4b800000, v53
	v_cmp_gt_f32_e64 s[0:1], s47, v53
	v_cmp_gt_f32_e32 vcc, s47, v52
	s_nop 0
	v_cndmask_b32_e64 v42, v53, v42, s[0:1]
	v_rsq_f32_e32 v42, v42
	s_nop 0
	v_mul_f32_e32 v43, 0x45800000, v42
	v_cndmask_b32_e64 v42, v42, v43, s[0:1]
	v_pk_mul_f32 v[54:55], v[56:57], v[42:43] op_sel_hi:[1,0]
	v_pk_mul_f32 v[48:49], v[48:49], v[42:43] op_sel_hi:[1,0]
	v_pk_mul_f32 v[54:55], v[94:95], v[54:55]
	v_pk_mul_f32 v[48:49], v[10:11], v[48:49]
	v_pk_mul_f32 v[44:45], v[44:45], v[54:55]
	v_pk_mul_f32 v[54:55], v[60:61], v[42:43] op_sel_hi:[1,0]
	v_pk_mul_f32 v[42:43], v[50:51], v[42:43] op_sel_hi:[1,0]
	v_pk_mul_f32 v[48:49], v[58:59], v[48:49]
	v_pk_mul_f32 v[42:43], v[2:3], v[42:43]
	v_pk_mul_f32 v[54:55], v[8:9], v[54:55]
	v_pk_mul_f32 v[42:43], v[62:63], v[42:43]
	v_pk_mul_f32 v[46:47], v[46:47], v[54:55]
	v_bfe_u32 v50, v43, 16, 1
	v_bfe_u32 v51, v42, 16, 1
	v_bfe_u32 v53, v49, 16, 1
	v_bfe_u32 v54, v48, 16, 1
	v_add3_u32 v48, v48, v54, s48
	v_add3_u32 v49, v49, v53, s48
	v_add3_u32 v42, v42, v51, s48
	v_add3_u32 v43, v43, v50, s48
	v_bfe_u32 v50, v44, 16, 1
	v_bfe_u32 v51, v45, 16, 1
	v_bfe_u32 v53, v46, 16, 1
	v_bfe_u32 v54, v47, 16, 1
	v_add3_u32 v47, v47, v54, s48
	v_add3_u32 v46, v46, v53, s48
	v_add3_u32 v45, v45, v51, s48
	v_add3_u32 v44, v44, v50, s48
	v_lshrrev_b32_e32 v50, 16, v44
	v_lshrrev_b32_e32 v51, 16, v45
	v_lshrrev_b32_e32 v44, 16, v46
	v_lshrrev_b32_e32 v45, 16, v47
	v_and_or_b32 v45, v43, s46, v45
	v_and_or_b32 v44, v42, s46, v44
	v_and_or_b32 v43, v49, s46, v51
	v_and_or_b32 v42, v48, s46, v50
	global_store_dwordx4 v[112:113], v[42:45], off
	v_lshlrev_b32_e32 v46, 16, v34
	v_and_b32_e32 v47, 0xffff0000, v35
	v_mul_f32_e32 v42, 0x4b800000, v52
	v_cndmask_b32_e32 v42, v52, v42, vcc
	v_rsq_f32_e32 v42, v42
	v_and_b32_e32 v48, 0xffff0000, v34
	v_mul_f32_e32 v34, 0xbfb8aa3b, v48
	v_exp_f32_e32 v34, v34
	v_mul_f32_e32 v43, 0x45800000, v42
	v_cndmask_b32_e32 v42, v42, v43, vcc
	v_pk_mul_f32 v[36:37], v[36:37], v[42:43] op_sel_hi:[1,0]
	v_pk_mul_f32 v[44:45], v[66:67], v[42:43] op_sel_hi:[1,0]
	v_pk_mul_f32 v[36:37], v[10:11], v[36:37]
	v_lshlrev_b32_e32 v43, 16, v35
	v_pk_mul_f32 v[36:37], v[40:41], v[36:37]
	v_mul_f32_e32 v40, 0xbfb8aa3b, v46
	v_mul_f32_e32 v35, 0xbfb8aa3b, v43
	v_exp_f32_e32 v40, v40
	v_exp_f32_e32 v41, v35
	v_pk_mul_f32 v[44:45], v[94:95], v[44:45]
	v_pk_add_f32 v[40:41], v[40:41], 1.0 op_sel_hi:[1,0]
	s_nop 0
	v_div_scale_f32 v35, s[0:1], v41, v41, v43
	v_rcp_f32_e32 v49, v35
	v_pk_mul_f32 v[32:33], v[32:33], v[44:45]
	v_pk_mul_f32 v[44:45], v[70:71], v[42:43] op_sel_hi:[1,0]
	v_fma_f32 v50, -v35, v49, 1.0
	v_fmac_f32_e32 v49, v50, v49
	v_div_scale_f32 v50, vcc, v43, v41, v43
	v_mul_f32_e32 v51, v50, v49
	v_fma_f32 v52, -v35, v51, v50
	v_fmac_f32_e32 v51, v52, v49
	v_fma_f32 v35, -v35, v51, v50
	v_div_fmas_f32 v35, v35, v49, v51
	v_div_fixup_f32 v41, v35, v41, v43
	v_div_scale_f32 v35, s[0:1], v40, v40, v46
	v_rcp_f32_e32 v43, v35
	v_pk_mul_f32 v[44:45], v[8:9], v[44:45]
	v_fma_f32 v49, -v35, v43, 1.0
	v_fmac_f32_e32 v43, v49, v43
	v_div_scale_f32 v49, vcc, v46, v40, v46
	v_mul_f32_e32 v50, v49, v43
	v_fma_f32 v51, -v35, v50, v49
	v_fmac_f32_e32 v50, v51, v43
	v_fma_f32 v35, -v35, v50, v49
	v_div_fmas_f32 v35, v35, v43, v50
	v_div_fixup_f32 v40, v35, v40, v46
	v_mul_f32_e32 v35, 0xbfb8aa3b, v47
	v_exp_f32_e32 v35, v35
	v_pk_mul_f32 v[38:39], v[38:39], v[42:43] op_sel_hi:[1,0]
	v_pk_mul_f32 v[40:41], v[40:41], v[44:45]
	v_pk_mul_f32 v[38:39], v[2:3], v[38:39]
	v_pk_add_f32 v[34:35], v[34:35], 1.0 op_sel_hi:[1,0]
	s_nop 0
	v_div_scale_f32 v42, s[0:1], v35, v35, v47
	v_rcp_f32_e32 v43, v42
	s_nop 0
	v_fma_f32 v44, -v42, v43, 1.0
	v_fmac_f32_e32 v43, v44, v43
	v_div_scale_f32 v44, vcc, v47, v35, v47
	v_mul_f32_e32 v45, v44, v43
	v_fma_f32 v46, -v42, v45, v44
	v_fmac_f32_e32 v45, v46, v43
	v_fma_f32 v42, -v42, v45, v44
	v_div_fmas_f32 v42, v42, v43, v45
	v_div_fixup_f32 v35, v42, v35, v47
	v_div_scale_f32 v42, s[0:1], v34, v34, v48
	v_rcp_f32_e32 v43, v42
	s_nop 0
	v_fma_f32 v44, -v42, v43, 1.0
	v_fmac_f32_e32 v43, v44, v43
	v_div_scale_f32 v44, vcc, v48, v34, v48
	v_mul_f32_e32 v45, v44, v43
	v_fma_f32 v46, -v42, v45, v44
	v_fmac_f32_e32 v45, v46, v43
	v_fma_f32 v42, -v42, v45, v44
	v_div_fmas_f32 v42, v42, v43, v45
	v_div_fixup_f32 v34, v42, v34, v48
	v_pk_mul_f32 v[34:35], v[34:35], v[38:39]
	v_bfe_u32 v42, v37, 16, 1
	v_bfe_u32 v38, v35, 16, 1
	v_bfe_u32 v39, v34, 16, 1
	v_bfe_u32 v43, v36, 16, 1
	v_add3_u32 v36, v36, v43, s48
	v_add3_u32 v37, v37, v42, s48
	v_add3_u32 v34, v34, v39, s48
	v_add3_u32 v35, v35, v38, s48
	v_bfe_u32 v38, v32, 16, 1
	v_bfe_u32 v39, v33, 16, 1
	v_bfe_u32 v42, v40, 16, 1
	v_bfe_u32 v43, v41, 16, 1
	v_add3_u32 v41, v41, v43, s48
	v_add3_u32 v40, v40, v42, s48
	v_add3_u32 v33, v33, v39, s48
	v_add3_u32 v32, v32, v38, s48
	v_lshrrev_b32_e32 v32, 16, v32
	v_lshrrev_b32_e32 v33, 16, v33
	v_lshrrev_b32_e32 v38, 16, v40
	v_lshrrev_b32_e32 v39, 16, v41
	v_and_or_b32 v35, v35, s46, v39
	v_and_or_b32 v34, v34, s46, v38
	v_and_or_b32 v33, v37, s46, v33
	v_and_or_b32 v32, v36, s46, v32
	v_and_b32_e32 v40, 0xffff0000, v20
	global_store_dwordx4 v[112:113], v[32:35], off offset:1024
	v_lshlrev_b32_e32 v37, 16, v21
	v_lshlrev_b32_e32 v38, 16, v20
	v_lshlrev_b32_e32 v33, 16, v29
	v_lshlrev_b32_e32 v32, 16, v28
	v_lshlrev_b32_e32 v35, 16, v25
	v_lshlrev_b32_e32 v34, 16, v24
	v_mul_f32_e32 v20, 0xbfb8aa3b, v40
	v_pk_add_f32 v[32:33], v[32:33], v[34:35]
	v_mul_f32_e32 v34, 0xbfb8aa3b, v38
	v_exp_f32_e32 v36, v20
	v_mul_f32_e32 v20, 0xbfb8aa3b, v37
	v_exp_f32_e32 v34, v34
	v_exp_f32_e32 v35, v20
	v_and_b32_e32 v39, 0xffff0000, v21
	v_and_b32_e32 v44, 0xffff0000, v22
	s_waitcnt vmcnt(6)
	v_and_b32_e32 v48, 0xffff0000, v4
	v_pk_add_f32 v[20:21], v[34:35], 1.0 op_sel_hi:[1,0]
	v_and_b32_e32 v29, 0xffff0000, v29
	v_div_scale_f32 v34, s[0:1], v21, v21, v37
	v_rcp_f32_e32 v35, v34
	v_and_b32_e32 v28, 0xffff0000, v28
	v_and_b32_e32 v25, 0xffff0000, v25
	v_and_b32_e32 v24, 0xffff0000, v24
	v_fma_f32 v41, -v34, v35, 1.0
	v_fmac_f32_e32 v35, v41, v35
	v_div_scale_f32 v41, vcc, v37, v21, v37
	v_mul_f32_e32 v42, v41, v35
	v_fma_f32 v43, -v34, v42, v41
	v_fmac_f32_e32 v42, v43, v35
	v_fma_f32 v34, -v34, v42, v41
	v_div_fmas_f32 v34, v34, v35, v42
	v_div_fixup_f32 v21, v34, v21, v37
	v_div_scale_f32 v34, s[0:1], v20, v20, v38
	v_rcp_f32_e32 v35, v34
	v_and_b32_e32 v43, 0xffff0000, v23
	v_pk_add_f32 v[24:25], v[28:29], v[24:25]
	v_pk_mul_f32 v[28:29], v[32:33], v[32:33]
	v_fma_f32 v37, -v34, v35, 1.0
	v_fmac_f32_e32 v35, v37, v35
	v_div_scale_f32 v37, vcc, v38, v20, v38
	v_mul_f32_e32 v41, v37, v35
	v_fma_f32 v42, -v34, v41, v37
	v_fmac_f32_e32 v41, v42, v35
	v_fma_f32 v34, -v34, v41, v37
	v_div_fmas_f32 v34, v34, v35, v41
	v_div_fixup_f32 v20, v34, v20, v38
	v_mul_f32_e32 v34, 0xbfb8aa3b, v39
	v_exp_f32_e32 v37, v34
	v_pk_fma_f32 v[28:29], v[24:25], v[24:25], v[28:29]
	v_pk_add_f32 v[34:35], v[36:37], 1.0 op_sel_hi:[1,0]
	s_nop 0
	v_div_scale_f32 v36, s[0:1], v35, v35, v39
	v_rcp_f32_e32 v37, v36
	s_nop 0
	v_fma_f32 v38, -v36, v37, 1.0
	v_fmac_f32_e32 v37, v38, v37
	v_div_scale_f32 v38, vcc, v39, v35, v39
	v_mul_f32_e32 v41, v38, v37
	v_fma_f32 v42, -v36, v41, v38
	v_fmac_f32_e32 v41, v42, v37
	v_fma_f32 v36, -v36, v41, v38
	v_div_fmas_f32 v36, v36, v37, v41
	v_div_fixup_f32 v35, v36, v35, v39
	v_div_scale_f32 v36, s[0:1], v34, v34, v40
	v_rcp_f32_e32 v37, v36
	v_lshlrev_b32_e32 v42, 16, v22
	v_mul_f32_e32 v22, 0xbfb8aa3b, v44
	v_fma_f32 v38, -v36, v37, 1.0
	v_fmac_f32_e32 v37, v38, v37
	v_div_scale_f32 v38, vcc, v40, v34, v40
	v_mul_f32_e32 v39, v38, v37
	v_fma_f32 v41, -v36, v39, v38
	v_fmac_f32_e32 v39, v41, v37
	v_fma_f32 v36, -v36, v39, v38
	v_div_fmas_f32 v36, v36, v37, v39
	v_div_fixup_f32 v34, v36, v34, v40
	v_lshlrev_b32_e32 v37, 16, v31
	v_lshlrev_b32_e32 v36, 16, v30
	v_lshlrev_b32_e32 v39, 16, v27
	v_lshlrev_b32_e32 v38, 16, v26
	v_lshlrev_b32_e32 v41, 16, v23
	v_pk_add_f32 v[36:37], v[36:37], v[38:39]
	v_mul_f32_e32 v38, 0xbfb8aa3b, v42
	v_exp_f32_e32 v40, v22
	v_mul_f32_e32 v22, 0xbfb8aa3b, v41
	v_exp_f32_e32 v38, v38
	v_exp_f32_e32 v39, v22
	v_and_b32_e32 v31, 0xffff0000, v31
	v_and_b32_e32 v30, 0xffff0000, v30
	v_and_b32_e32 v27, 0xffff0000, v27
	v_pk_add_f32 v[22:23], v[38:39], 1.0 op_sel_hi:[1,0]
	v_and_b32_e32 v26, 0xffff0000, v26
	v_div_scale_f32 v38, s[0:1], v23, v23, v41
	v_rcp_f32_e32 v39, v38
	v_pk_add_f32 v[26:27], v[30:31], v[26:27]
	v_pk_mul_f32 v[30:31], v[36:37], v[36:37]
	v_fma_f32 v45, -v38, v39, 1.0
	v_fmac_f32_e32 v39, v45, v39
	v_div_scale_f32 v45, vcc, v41, v23, v41
	v_mul_f32_e32 v46, v45, v39
	v_fma_f32 v47, -v38, v46, v45
	v_fmac_f32_e32 v46, v47, v39
	v_fma_f32 v38, -v38, v46, v45
	v_div_fmas_f32 v38, v38, v39, v46
	v_div_fixup_f32 v23, v38, v23, v41
	v_div_scale_f32 v38, s[0:1], v22, v22, v42
	v_rcp_f32_e32 v39, v38
	v_and_b32_e32 v47, 0xffff0000, v5
	v_pk_fma_f32 v[30:31], v[26:27], v[26:27], v[30:31]
	v_fma_f32 v41, -v38, v39, 1.0
	v_fmac_f32_e32 v39, v41, v39
	v_div_scale_f32 v41, vcc, v42, v22, v42
	v_mul_f32_e32 v45, v41, v39
	v_fma_f32 v46, -v38, v45, v41
	v_fmac_f32_e32 v45, v46, v39
	v_fma_f32 v38, -v38, v45, v41
	v_div_fmas_f32 v38, v38, v39, v45
	v_div_fixup_f32 v22, v38, v22, v42
	v_mul_f32_e32 v38, 0xbfb8aa3b, v43
	v_exp_f32_e32 v41, v38
	s_nop 0
	v_pk_add_f32 v[38:39], v[40:41], 1.0 op_sel_hi:[1,0]
	s_nop 0
	v_div_scale_f32 v40, s[0:1], v39, v39, v43
	v_rcp_f32_e32 v41, v40
	s_nop 0
	v_fma_f32 v42, -v40, v41, 1.0
	v_fmac_f32_e32 v41, v42, v41
	v_div_scale_f32 v42, vcc, v43, v39, v43
	v_mul_f32_e32 v45, v42, v41
	v_fma_f32 v46, -v40, v45, v42
	v_fmac_f32_e32 v45, v46, v41
	v_fma_f32 v40, -v40, v45, v42
	v_div_fmas_f32 v40, v40, v41, v45
	v_div_fixup_f32 v39, v40, v39, v43
	v_div_scale_f32 v40, s[0:1], v38, v38, v44
	v_rcp_f32_e32 v41, v40
	v_lshlrev_b32_e32 v46, 16, v4
	v_mul_f32_e32 v4, 0xbfb8aa3b, v48
	v_fma_f32 v42, -v40, v41, 1.0
	v_fmac_f32_e32 v41, v42, v41
	v_div_scale_f32 v42, vcc, v44, v38, v44
	v_mul_f32_e32 v43, v42, v41
	v_fma_f32 v45, -v40, v43, v42
	v_fmac_f32_e32 v43, v45, v41
	v_fma_f32 v40, -v40, v43, v42
	v_div_fmas_f32 v40, v40, v41, v43
	v_div_fixup_f32 v38, v40, v38, v44
	v_lshlrev_b32_e32 v41, 16, v17
	v_lshlrev_b32_e32 v40, 16, v16
	v_lshlrev_b32_e32 v43, 16, v13
	v_lshlrev_b32_e32 v42, 16, v12
	v_pk_add_f32 v[40:41], v[40:41], v[42:43]
	v_and_b32_e32 v17, 0xffff0000, v17
	v_and_b32_e32 v16, 0xffff0000, v16
	v_and_b32_e32 v13, 0xffff0000, v13
	v_and_b32_e32 v12, 0xffff0000, v12
	v_pk_add_f32 v[42:43], v[16:17], v[12:13]
	v_pk_mul_f32 v[12:13], v[40:41], v[40:41]
	v_lshlrev_b32_e32 v45, 16, v5
	v_pk_fma_f32 v[16:17], v[42:43], v[42:43], v[12:13]
	v_mul_f32_e32 v12, 0xbfb8aa3b, v46
	v_exp_f32_e32 v44, v4
	v_mul_f32_e32 v4, 0xbfb8aa3b, v45
	v_exp_f32_e32 v12, v12
	v_exp_f32_e32 v13, v4
	s_nop 0
	v_pk_add_f32 v[4:5], v[12:13], 1.0 op_sel_hi:[1,0]
	s_nop 0
	v_div_scale_f32 v12, s[0:1], v5, v5, v45
	v_rcp_f32_e32 v13, v12
	s_nop 0
	v_fma_f32 v49, -v12, v13, 1.0
	v_fmac_f32_e32 v13, v49, v13
	v_div_scale_f32 v49, vcc, v45, v5, v45
	v_mul_f32_e32 v50, v49, v13
	v_fma_f32 v51, -v12, v50, v49
	v_fmac_f32_e32 v50, v51, v13
	v_fma_f32 v12, -v12, v50, v49
	v_div_fmas_f32 v12, v12, v13, v50
	v_div_fixup_f32 v5, v12, v5, v45
	v_div_scale_f32 v12, s[0:1], v4, v4, v46
	v_rcp_f32_e32 v13, v12
	s_nop 0
	v_fma_f32 v45, -v12, v13, 1.0
	v_fmac_f32_e32 v13, v45, v13
	v_div_scale_f32 v45, vcc, v46, v4, v46
	v_mul_f32_e32 v49, v45, v13
	v_fma_f32 v50, -v12, v49, v45
	v_fmac_f32_e32 v49, v50, v13
	v_fma_f32 v12, -v12, v49, v45
	v_div_fmas_f32 v12, v12, v13, v49
	v_div_fixup_f32 v4, v12, v4, v46
	v_mul_f32_e32 v12, 0xbfb8aa3b, v47
	v_exp_f32_e32 v45, v12
	s_nop 0
	v_pk_add_f32 v[12:13], v[44:45], 1.0 op_sel_hi:[1,0]
	s_nop 0
	v_div_scale_f32 v44, s[0:1], v13, v13, v47
	v_rcp_f32_e32 v45, v44
	s_nop 0
	v_fma_f32 v46, -v44, v45, 1.0
	v_fmac_f32_e32 v45, v46, v45
	v_div_scale_f32 v46, vcc, v47, v13, v47
	v_mul_f32_e32 v49, v46, v45
	v_fma_f32 v50, -v44, v49, v46
	v_fmac_f32_e32 v49, v50, v45
	v_fma_f32 v44, -v44, v49, v46
	v_div_fmas_f32 v44, v44, v45, v49
	v_div_fixup_f32 v45, v44, v13, v47
	v_div_scale_f32 v13, s[0:1], v12, v12, v48
	v_rcp_f32_e32 v44, v13
	s_nop 0
	v_fma_f32 v46, -v13, v44, 1.0
	v_fmac_f32_e32 v44, v46, v44
	v_div_scale_f32 v46, vcc, v48, v12, v48
	v_mul_f32_e32 v47, v46, v44
	v_fma_f32 v49, -v13, v47, v46
	v_fmac_f32_e32 v47, v49, v44
	v_fma_f32 v13, -v13, v47, v46
	v_div_fmas_f32 v13, v13, v44, v47
	v_div_fixup_f32 v44, v13, v12, v48
	v_lshlrev_b32_e32 v13, 16, v19
	v_lshlrev_b32_e32 v12, 16, v18
	v_lshlrev_b32_e32 v47, 16, v15
	v_lshlrev_b32_e32 v46, 16, v14
	v_pk_add_f32 v[12:13], v[12:13], v[46:47]
	v_and_b32_e32 v19, 0xffff0000, v19
	v_and_b32_e32 v18, 0xffff0000, v18
	v_and_b32_e32 v15, 0xffff0000, v15
	v_and_b32_e32 v14, 0xffff0000, v14
	v_pk_add_f32 v[14:15], v[18:19], v[14:15]
	v_pk_mul_f32 v[18:19], v[12:13], v[12:13]
	v_mov_b32_e32 v46, v16
	v_pk_fma_f32 v[18:19], v[14:15], v[14:15], v[18:19]
	v_mov_b32_e32 v47, v28
	v_mov_b32_e32 v28, v17
	v_pk_add_f32 v[16:17], v[46:47], v[28:29]
	v_mov_b32_e32 v28, v18
	v_mov_b32_e32 v29, v30
	v_pk_add_f32 v[16:17], v[28:29], v[16:17]
	v_mov_b32_e32 v30, v19
	v_pk_add_f32 v[16:17], v[30:31], v[16:17]
	ds_swizzle_b32 v19, v17 offset:swizzle(SWAP,1)
	ds_swizzle_b32 v18, v16 offset:swizzle(SWAP,1)
	s_waitcnt lgkmcnt(0)
	v_pk_add_f32 v[16:17], v[16:17], v[18:19]
	ds_swizzle_b32 v19, v17 offset:swizzle(SWAP,2)
	ds_swizzle_b32 v18, v16 offset:swizzle(SWAP,2)
	s_waitcnt lgkmcnt(0)
	v_pk_add_f32 v[16:17], v[16:17], v[18:19]
	ds_swizzle_b32 v19, v17 offset:swizzle(SWAP,4)
	ds_swizzle_b32 v18, v16 offset:swizzle(SWAP,4)
	s_waitcnt lgkmcnt(0)
	v_pk_add_f32 v[16:17], v[16:17], v[18:19]
	ds_swizzle_b32 v19, v17 offset:swizzle(SWAP,8)
	ds_swizzle_b32 v18, v16 offset:swizzle(SWAP,8)
	s_waitcnt lgkmcnt(0)
	v_pk_add_f32 v[16:17], v[16:17], v[18:19]
	ds_swizzle_b32 v19, v17 offset:swizzle(SWAP,16)
	ds_swizzle_b32 v18, v16 offset:swizzle(SWAP,16)
	s_waitcnt lgkmcnt(0)
	v_pk_add_f32 v[16:17], v[16:17], v[18:19]
	s_nop 0
	v_pk_fma_f32 v[0:1], v[16:17], s[30:31], v[0:1] op_sel_hi:[1,0,0]
	s_nop 0
	v_mul_f32_e32 v16, 0x4b800000, v1
	v_cmp_gt_f32_e64 s[0:1], s47, v1
	v_cmp_gt_f32_e32 vcc, s47, v0
	s_nop 0
	v_cndmask_b32_e64 v1, v1, v16, s[0:1]
	v_rsq_f32_e32 v1, v1
	s_nop 0
	v_mul_f32_e32 v16, 0x45800000, v1
	v_cndmask_b32_e64 v16, v1, v16, s[0:1]
	v_pk_mul_f32 v[18:19], v[32:33], v[16:17] op_sel_hi:[1,0]
	s_nop 0
	v_pk_mul_f32 v[18:19], v[94:95], v[18:19]
	s_nop 0
	v_pk_mul_f32 v[18:19], v[20:21], v[18:19]
	v_pk_mul_f32 v[20:21], v[24:25], v[16:17] op_sel_hi:[1,0]
	v_pk_mul_f32 v[24:25], v[36:37], v[16:17] op_sel_hi:[1,0]
	v_pk_mul_f32 v[16:17], v[26:27], v[16:17] op_sel_hi:[1,0]
	v_pk_mul_f32 v[20:21], v[10:11], v[20:21]
	v_pk_mul_f32 v[16:17], v[2:3], v[16:17]
	v_pk_mul_f32 v[20:21], v[34:35], v[20:21]
	v_pk_mul_f32 v[24:25], v[8:9], v[24:25]
	v_pk_mul_f32 v[16:17], v[38:39], v[16:17]
	v_pk_mul_f32 v[22:23], v[22:23], v[24:25]
	v_bfe_u32 v1, v17, 16, 1
	v_bfe_u32 v24, v16, 16, 1
	v_bfe_u32 v26, v20, 16, 1
	v_add3_u32 v20, v20, v26, s48
	v_add3_u32 v16, v16, v24, s48
	v_add3_u32 v1, v17, v1, s48
	v_bfe_u32 v17, v18, 16, 1
	v_bfe_u32 v24, v19, 16, 1
	v_bfe_u32 v26, v23, 16, 1
	v_add3_u32 v23, v23, v26, s48
	v_add3_u32 v19, v19, v24, s48
	v_add3_u32 v17, v18, v17, s48
	v_lshrrev_b32_e32 v24, 16, v17
	v_lshrrev_b32_e32 v17, 16, v19
	v_lshrrev_b32_e32 v19, 16, v23
	v_and_or_b32 v19, v1, s46, v19
	v_mul_f32_e32 v1, 0x4b800000, v0
	v_cndmask_b32_e32 v0, v0, v1, vcc
	v_bfe_u32 v25, v21, 16, 1
	v_rsq_f32_e32 v0, v0
	v_add3_u32 v21, v21, v25, s48
	v_bfe_u32 v25, v22, 16, 1
	v_add3_u32 v22, v22, v25, s48
	v_lshrrev_b32_e32 v18, 16, v22
	v_and_or_b32 v18, v16, s46, v18
	v_and_or_b32 v17, v21, s46, v17
	v_and_or_b32 v16, v20, s46, v24
	v_mul_f32_e32 v1, 0x45800000, v0
	global_store_dwordx4 v[112:113], v[16:19], off offset:2048
	v_lshlrev_b32_e32 v21, 16, v6
	v_and_b32_e32 v20, 0xffff0000, v7
	v_cndmask_b32_e32 v16, v0, v1, vcc
	v_pk_mul_f32 v[0:1], v[40:41], v[16:17] op_sel_hi:[1,0]
	s_nop 0
	v_pk_mul_f32 v[0:1], v[94:95], v[0:1]
	s_nop 0
	v_pk_mul_f32 v[0:1], v[4:5], v[0:1]
	v_pk_mul_f32 v[4:5], v[42:43], v[16:17] op_sel_hi:[1,0]
	v_and_b32_e32 v17, 0xffff0000, v6
	v_pk_mul_f32 v[4:5], v[10:11], v[4:5]
	v_mul_f32_e32 v10, 0xbfb8aa3b, v21
	v_mul_f32_e32 v6, 0xbfb8aa3b, v17
	v_lshlrev_b32_e32 v11, 16, v7
	v_exp_f32_e32 v18, v10
	v_exp_f32_e32 v10, v6
	v_pk_mul_f32 v[6:7], v[12:13], v[16:17] op_sel_hi:[1,0]
	v_pk_mul_f32 v[4:5], v[44:45], v[4:5]
	v_pk_mul_f32 v[6:7], v[8:9], v[6:7]
	v_mul_f32_e32 v8, 0xbfb8aa3b, v11
	v_exp_f32_e32 v19, v8
	s_nop 0
	v_pk_add_f32 v[8:9], v[18:19], 1.0 op_sel_hi:[1,0]
	s_nop 0
	v_div_scale_f32 v12, s[0:1], v9, v9, v11
	v_rcp_f32_e32 v13, v12
	s_nop 0
	v_fma_f32 v18, -v12, v13, 1.0
	v_fmac_f32_e32 v13, v18, v13
	v_div_scale_f32 v18, vcc, v11, v9, v11
	v_mul_f32_e32 v19, v18, v13
	v_fma_f32 v22, -v12, v19, v18
	v_fmac_f32_e32 v19, v22, v13
	v_fma_f32 v12, -v12, v19, v18
	v_div_fmas_f32 v12, v12, v13, v19
	v_div_fixup_f32 v9, v12, v9, v11
	v_div_scale_f32 v11, s[0:1], v8, v8, v21
	v_rcp_f32_e32 v12, v11
	s_nop 0
	v_fma_f32 v13, -v11, v12, 1.0
	v_fmac_f32_e32 v12, v13, v12
	v_div_scale_f32 v13, vcc, v21, v8, v21
	v_mul_f32_e32 v18, v13, v12
	v_fma_f32 v19, -v11, v18, v13
	v_fmac_f32_e32 v18, v19, v12
	v_fma_f32 v11, -v11, v18, v13
	v_div_fmas_f32 v11, v11, v12, v18
	v_div_fixup_f32 v8, v11, v8, v21
	v_pk_mul_f32 v[6:7], v[8:9], v[6:7]
	v_pk_mul_f32 v[8:9], v[14:15], v[16:17] op_sel_hi:[1,0]
	s_nop 0
	v_pk_mul_f32 v[2:3], v[2:3], v[8:9]
	v_mul_f32_e32 v8, 0xbfb8aa3b, v20
	v_exp_f32_e32 v11, v8
	s_nop 0
	v_pk_add_f32 v[8:9], v[10:11], 1.0 op_sel_hi:[1,0]
	s_nop 0
	v_div_scale_f32 v10, s[0:1], v9, v9, v20
	v_rcp_f32_e32 v11, v10
	s_nop 0
	v_fma_f32 v12, -v10, v11, 1.0
	v_fmac_f32_e32 v11, v12, v11
	v_div_scale_f32 v12, vcc, v20, v9, v20
	v_mul_f32_e32 v13, v12, v11
	v_fma_f32 v14, -v10, v13, v12
	v_fmac_f32_e32 v13, v14, v11
	v_fma_f32 v10, -v10, v13, v12
	v_div_fmas_f32 v10, v10, v11, v13
	v_div_fixup_f32 v9, v10, v9, v20
	v_div_scale_f32 v10, s[0:1], v8, v8, v17
	v_rcp_f32_e32 v11, v10
	s_nop 0
	v_fma_f32 v12, -v10, v11, 1.0
	v_fmac_f32_e32 v11, v12, v11
	v_div_scale_f32 v12, vcc, v17, v8, v17
	v_mul_f32_e32 v13, v12, v11
	v_fma_f32 v14, -v10, v13, v12
	v_fmac_f32_e32 v13, v14, v11
	v_fma_f32 v10, -v10, v13, v12
	v_div_fmas_f32 v10, v10, v11, v13
	v_div_fixup_f32 v8, v10, v8, v17
	v_pk_mul_f32 v[2:3], v[8:9], v[2:3]
	v_bfe_u32 v10, v5, 16, 1
	v_bfe_u32 v8, v3, 16, 1
	v_bfe_u32 v9, v2, 16, 1
	v_bfe_u32 v11, v4, 16, 1
	v_add3_u32 v4, v4, v11, s48
	v_add3_u32 v5, v5, v10, s48
	v_add3_u32 v2, v2, v9, s48
	v_add3_u32 v3, v3, v8, s48
	v_bfe_u32 v8, v0, 16, 1
	v_bfe_u32 v9, v1, 16, 1
	v_bfe_u32 v10, v6, 16, 1
	v_bfe_u32 v11, v7, 16, 1
	v_add3_u32 v7, v7, v11, s48
	v_add3_u32 v6, v6, v10, s48
	v_add3_u32 v1, v1, v9, s48
	v_add3_u32 v0, v0, v8, s48
	v_lshrrev_b32_e32 v0, 16, v0
	v_lshrrev_b32_e32 v1, 16, v1
	v_lshrrev_b32_e32 v6, 16, v6
	v_lshrrev_b32_e32 v7, 16, v7
	v_and_or_b32 v3, v3, s46, v7
	v_and_or_b32 v2, v2, s46, v6
	v_and_or_b32 v1, v5, s46, v1
	v_and_or_b32 v0, v4, s46, v0
	global_store_dwordx4 v[112:113], v[0:3], off offset:3072
	s_cbranch_scc1 .LBB0_565
